# GLA chunk S1 emitted straight-line (fma exponent, running LDS address, cvt_pk rounding); fp8 weight conversion items all on the GLA workgroups
# speedup vs baseline: 1.0294x; 1.0294x over previous
; __device__ __forceinline__ unsigned xb_ld(unsigned* p)              { return __hip_atomic_load(p, __ATOMIC_RELAXED, __HIP_MEMORY_SCOPE_AGENT); }
; __device__ __forceinline__ CArgs* kargs() { CArgs* p = (CArgs*)__builtin_amdgcn_kernarg_segment_ptr(); asm volatile("" : "+s"(p)); return p; }
; #define PB_BEG(ty) do { if (PROBE_PH == (ty)) tbeg = __builtin_amdgcn_s_memrealtime(); } while (0)
; __device__ __forceinline__ void xcd_barrier_complete(unsigned* bar, unsigned x, unsigned& nloc, unsigned& nx) {
;     const unsigned G = gridDim.x * gridDim.y * gridDim.z;
;     unsigned sum, cnt, mine, sp = 0u;
;     for (;;) {
;         sum = 0u; cnt = 0u; mine = 0u;
; #pragma unroll
;         for (unsigned j = 0; j < 16; ++j) { const unsigned c = xb_ld(&bar[XB_XCNT(j)]); sum += c; cnt += (c > 0u) ? 1u : 0u; mine = (j == x) ? c : mine; }
;         if (sum == G) break;
;         __builtin_amdgcn_s_sleep(1);
;         if ((++sp & 255u) == 0u) { if (xb_ld(&bar[XB_TMO])) break; if (sp > XB_SPIN_CAP) { atomicAdd(&bar[XB_TMO], 1u); break; } }
;     }
;     nloc = mine > 0u ? mine : 1u; nx = cnt > 0u ? cnt : 1u;
; }
; __global__ void __launch_bounds__(512, 2) trunk_fwd(Args a_unused) {
;     ...
; #pragma unroll 1
;     for (int l = 0; l < DEPTH; ++l) {
;         const int p0 = 2 + 9 * l;
;         const bool lastl = (l == DEPTH - 1);
;         PB_BEG(2);
;         if (IN(p0 + 0)) {
;             CArgs& a = *kargs();
;             pg8::DenseSched S; S.init((const bf16*)(a.ws + WS_WIN) + (size_t)l * D_INP * 1024, 1024, NTOK, D_INP, nblk, bid, 0);
.LBB0_186:
	s_cmpk_lt_i32 s64, 0x7e0
	s_cselect_b64 s[2:3], -1, 0
	s_ashr_i32 s69, s64, 31
	s_lshr_b32 s1, s69, 29
	s_add_i32 s1, s64, s1
	s_ashr_i32 s8, s1, 3
	s_and_b32 s1, s1, -8
	v_writelane_b32 v251, s2, 16
	s_sub_i32 s9, s64, s1
	s_ashr_i32 s74, s68, 31
	v_writelane_b32 v251, s3, 17
	s_add_u32 s2, s80, 0x4200
	s_addc_u32 s3, s81, 0
	s_add_u32 s86, s80, 0x4400
	s_addc_u32 s87, s81, 0
	s_add_u32 s88, s80, 0x4500
	s_addc_u32 s89, s81, 0
	s_add_u32 s90, s80, 0x4600
	s_addc_u32 s91, s81, 0
	s_add_u32 s92, s80, 0x4700
	s_addc_u32 s93, s81, 0
	s_add_u32 s94, s80, 0x4800
	s_addc_u32 s95, s81, 0
	s_add_u32 s96, s80, 0x4900
	s_addc_u32 s97, s81, 0
	s_add_u32 s72, s80, 0x4a00
	s_addc_u32 s73, s81, 0
	s_add_u32 s60, s80, 0x4b00
	v_writelane_b32 v251, s2, 18
	s_addc_u32 s61, s81, 0
	v_mbcnt_lo_u32_b32 v1, -1, 0
	v_writelane_b32 v251, s3, 19
	s_add_u32 s2, s80, 0x4c00
	s_addc_u32 s3, s81, 0
	v_writelane_b32 v251, s2, 20
	s_mov_b32 s79, 0
	v_mov_b32_e32 v35, 0
	v_writelane_b32 v251, s3, 21
	s_add_u32 s2, s80, 0x4d00
	s_addc_u32 s3, s81, 0
	v_writelane_b32 v251, s2, 22
	v_mov_b32_e32 v169, 1
	v_mov_b32_e32 v190, 0x3727c5ac
	v_writelane_b32 v251, s3, 23
	s_add_u32 s2, s80, 0x4e00
	s_addc_u32 s3, s81, 0
	v_writelane_b32 v251, s2, 24
	v_mov_b32_e32 v191, 0x7f7f7f7f
	v_mov_b64_e32 v[164:165], 0x7e0
	v_writelane_b32 v251, s3, 25
	s_add_u32 s2, s80, 0x4f00
	s_addc_u32 s3, s81, 0
	v_writelane_b32 v251, s2, 26
	v_mov_b64_e32 v[166:167], 0x7df
	v_mov_b32_e32 v192, 0x1a40
	v_writelane_b32 v251, s3, 27
	s_add_u32 s2, s80, 0x5000
	s_addc_u32 s3, s81, 0
	v_writelane_b32 v251, s2, 28
	v_mov_b32_e32 v193, 0x41b17218
	v_mov_b32_e32 v194, 0x3e3504f3
	v_writelane_b32 v251, s3, 29
	s_add_u32 s2, s80, 0x5100
	s_addc_u32 s3, s81, 0
	v_writelane_b32 v251, s2, 30
	v_mbcnt_hi_u32_b32 v195, -1, v1
	v_mov_b32_e32 v196, 0x3fb8aa3b
	v_writelane_b32 v251, s3, 31
	s_add_u32 s2, s80, 0x5200
	s_addc_u32 s3, s81, 0
	v_writelane_b32 v251, s2, 32
	v_mov_b32_e32 v197, 0x1ff
	v_mov_b32_e32 v198, 0xfff
	v_writelane_b32 v251, s3, 33
	s_add_u32 s2, s80, 0x5300
	s_addc_u32 s3, s81, 0
	v_writelane_b32 v251, s2, 34
	s_cmp_eq_u32 s48, 15
	v_mov_b32_e32 v168, 0x358637bd
	v_writelane_b32 v251, s3, 35
	s_cselect_b64 s[2:3], -1, 0
	v_writelane_b32 v251, s2, 36
	s_cmp_eq_u32 s48, 14
	v_mov_b32_e32 v199, 0xff61b1e6
	v_writelane_b32 v251, s3, 37
	s_cselect_b64 s[2:3], -1, 0
	v_writelane_b32 v251, s2, 38
	s_cmp_eq_u32 s48, 13
	v_mov_b32_e32 v200, 0x40e00000
	v_writelane_b32 v251, s3, 39
	s_cselect_b64 s[2:3], -1, 0
	v_writelane_b32 v251, s2, 40
	s_cmp_eq_u32 s48, 12
	v_mov_b32_e32 v201, 0x43e00000
	v_writelane_b32 v251, s3, 41
	s_cselect_b64 s[2:3], -1, 0
	v_writelane_b32 v251, s2, 42
	s_cmp_eq_u32 s48, 11
	s_movk_i32 s65, 0x1c00
	v_writelane_b32 v251, s3, 43
	s_cselect_b64 s[2:3], -1, 0
	v_writelane_b32 v251, s2, 44
	s_cmp_eq_u32 s48, 10
	s_movk_i32 s75, 0x90
	v_writelane_b32 v251, s3, 45
	s_cselect_b64 s[2:3], -1, 0
	v_writelane_b32 v251, s2, 46
	s_cmp_eq_u32 s48, 9
	s_mov_b32 s21, 0x800000
	v_writelane_b32 v251, s3, 47
	s_cselect_b64 s[2:3], -1, 0
	v_writelane_b32 v251, s2, 48
	s_cmp_eq_u32 s48, 8
	s_mov_b64 s[62:63], 0x40000
	v_writelane_b32 v251, s3, 49
	s_cselect_b64 s[2:3], -1, 0
	v_writelane_b32 v251, s2, 50
	s_cmp_eq_u32 s48, 7
	s_mov_b64 s[24:25], 0x80
	v_writelane_b32 v251, s3, 51
	s_cselect_b64 s[2:3], -1, 0
	v_writelane_b32 v251, s2, 52
	s_cmp_eq_u32 s48, 6
	s_mov_b64 s[40:41], 0x20080
	v_writelane_b32 v251, s3, 53
	s_cselect_b64 s[2:3], -1, 0
	v_writelane_b32 v251, s2, 54
	s_cmp_eq_u32 s48, 5
	s_mov_b64 s[66:67], 0x800
	v_writelane_b32 v251, s3, 55
	s_cselect_b64 s[2:3], -1, 0
	v_writelane_b32 v251, s2, 56
	s_cmp_eq_u32 s48, 4
	s_mov_b64 s[76:77], 0x30080
	v_writelane_b32 v251, s3, 57
	s_cselect_b64 s[2:3], -1, 0
	v_writelane_b32 v251, s2, 58
	s_cmp_eq_u32 s48, 3
	s_mov_b32 s84, s79
	v_writelane_b32 v251, s3, 59
	s_cselect_b64 s[2:3], -1, 0
	v_writelane_b32 v251, s2, 60
	s_cmp_eq_u32 s48, 2
	s_nop 0
	v_writelane_b32 v251, s3, 61
	s_cselect_b64 s[2:3], -1, 0
	v_writelane_b32 v251, s2, 62
	s_cmp_eq_u32 s48, 1
	s_nop 0
	v_writelane_b32 v251, s3, 63
	s_cselect_b64 s[2:3], -1, 0
	v_writelane_b32 v252, s2, 0
	s_cmp_eq_u32 s48, 0
	v_readlane_b32 s14, v251, 5
	v_writelane_b32 v252, s3, 1
	s_cselect_b64 s[2:3], -1, 0
	s_lshl_b32 s1, s48, 8
	v_writelane_b32 v252, s2, 2
	s_add_u32 s1, s80, s1
	v_readlane_b32 s15, v251, 6
	v_writelane_b32 v252, s3, 3
	s_addc_u32 s2, s81, 0
	s_add_u32 s4, s1, 0x5400
	s_addc_u32 s5, s2, 0
	v_writelane_b32 v252, s4, 4
	s_nop 1
	v_writelane_b32 v252, s5, 5
	s_add_u32 s4, s1, 0x6400
	s_addc_u32 s5, s2, 0
	v_writelane_b32 v252, s4, 6
	s_add_u32 s2, s80, 0x7400
	s_addc_u32 s3, s81, 0
	v_writelane_b32 v252, s5, 7
	v_writelane_b32 v252, s2, 8
	s_nop 1
	v_writelane_b32 v252, s3, 9
	s_add_u32 s2, s80, 0x7500
	s_addc_u32 s3, s81, 0
	s_not_b32 s1, s0
	s_waitcnt lgkmcnt(0)
; #define LAS __attribute__((address_space(3)))
; __device__ __forceinline__ void cvb_load(CArgs& a, int l, int bit, int w, int lane, CvbRegs& r) {
;     const int kbb = bit & 7, nb = (bit >> 3) & 3, m = bit >> 5, e = m / 3, which = m - 3 * e;
;     const float* W = a.in[which == 0 ? I_WG : (which == 1 ? I_WU : I_WD)] + ((size_t)(l * NEXP + e)) * 1024 * 1024 + (size_t)(128 * kbb + 16 * w) * 1024 + 256 * nb + 4 * lane;
; __device__ __forceinline__ void ph_scan(CArgs& a, int l, LAS unsigned char* lds, int bid, int nblk, unsigned long long& tacc) {
;     ...
;     {
;         LAS unsigned char* scr = lds + w * 8448;
;         if (nblk == 256) { const int per = bid < 128 ? 8 : 16, first = bid < 128 ? bid * 8 : 1024 + (bid - 128) * 16;
;             CvbRegs r0, r1;
;             cvb_load(a, l, first, w, lane, r0);
; #pragma unroll 1
;             for (int it = first; it < first + per; it += 2) {
;                 cvb_load(a, l, it + 1, w, lane, r1);
;                 cvb_store(a, it, w, lane, r0, lds);
;                 cvb_load(a, l, min(it + 2, first + per - 1), w, lane, r0);
;                 cvb_store(a, it + 1, w, lane, r1, lds + 36864); } }
;         else tr_experts_range(a, l, scr, bid * 8 + w, NEXP * 3 * 512, nblk * 8, lane);
	s_add_i32 s10, s14, s1
	v_writelane_b32 v252, s2, 10
	s_cmpk_lt_i32 s10, 0x2400
	s_mov_b32 s80, 0xffff0000
	v_writelane_b32 v252, s3, 11
	s_cselect_b64 s[2:3], -1, 0
	v_writelane_b32 v252, s2, 12
	s_lshl_b32 s12, s68, 5
	s_movk_i32 s81, 0x7fff
	v_writelane_b32 v252, s3, 13
	s_lshl_b32 s2, s10, 2
	s_cmpk_lt_i32 s64, 0x100
	s_cselect_b64 s[4:5], -1, 0
	v_writelane_b32 v252, s4, 14
	s_cmpk_lg_i32 s68, 0x100
	s_nop 0
	v_writelane_b32 v252, s5, 15
	s_cselect_b64 s[4:5], -1, 0
	v_writelane_b32 v252, s4, 16
	s_cmpk_gt_i32 s64, 0x7f
	s_nop 0
	v_writelane_b32 v252, s5, 17
	s_cselect_b64 s[4:5], -1, 0
	v_writelane_b32 v252, s4, 18
	s_lshl_b32 s1, s64, 1
	s_add_i32 s3, s1, 0xffffff00
	v_writelane_b32 v252, s5, 19
	s_add_i32 s4, s64, 0x200
	v_writelane_b32 v252, s4, 20
	v_writelane_b32 v252, s3, 21
	s_lshl_b32 s3, s3, 4
	s_addk_i32 s1, 0xff01
	v_writelane_b32 v252, s3, 22
	s_lshl_b32 s4, s64, 4
	v_writelane_b32 v252, s1, 23
	s_lshl_b32 s1, s1, 4
	v_writelane_b32 v252, s1, 24
	s_add_i32 s1, s4, 0xfffffc00
	s_mul_i32 s1, s64, 24
	s_addk_i32 s1, 0xf400
	s_cmpk_lt_i32 s64, 0x80
	v_readlane_b32 s3, v251, 4
	s_cselect_b32 s11, s3, s1
	s_cselect_b32 s3, 8, 24
	s_ashr_i32 s1, s11, 5
	v_writelane_b32 v252, s4, 25
	s_mul_hi_i32 s4, s1, 0x55555556
	s_lshr_b32 s5, s4, 31
	s_add_i32 s4, s4, s5
	v_writelane_b32 v252, s4, 26
	s_mul_i32 s4, s4, -3
	s_add_i32 s4, s4, s1
	s_cmp_eq_u32 s4, 1
	s_cselect_b32 s1, 33, 35
	s_cmp_lg_u32 s4, 0
	s_cselect_b32 s1, s1, 31
	s_lshl_b32 s4, s11, 5
	s_add_i32 s5, s11, s3
	s_ashr_i32 s3, s68, 3
	v_writelane_b32 v252, s4, 27
	s_mul_i32 s3, s3, s9
	v_writelane_b32 v252, s5, 28
	s_add_i32 s5, s5, -1
	s_add_i32 s3, s3, s8
	s_and_b32 s4, s4, 0x300
	v_writelane_b32 v252, s5, 29
	s_and_b32 s5, s68, 7
	s_lshl_b32 s6, s0, 1
	s_lshl_b32 s36, s68, 4
	s_cmp_lt_i32 s9, 0
	v_writelane_b32 v252, s6, 30
	s_cselect_b64 s[6:7], -1, 0
	v_writelane_b32 v252, s6, 31
	s_nop 1
	v_writelane_b32 v252, s7, 32
	s_and_b64 s[6:7], s[6:7], exec
	s_movk_i32 s6, 0xfd
	s_cselect_b32 s6, s6, 0xfc
	s_mul_i32 s6, s9, s6
	s_add_i32 s6, s6, s8
	s_mul_hi_i32 s7, s6, 0x92492493
	v_writelane_b32 v252, s9, 33
	s_add_i32 s7, s7, s6
	v_writelane_b32 v252, s8, 34
	s_lshr_b32 s8, s7, 31
	s_ashr_i32 s7, s7, 6
	s_add_i32 s7, s7, s8
	s_mul_i32 s8, s7, 0x70
	s_sub_i32 s6, s6, s8
	s_bfe_i32 s8, s6, 0x80000
	s_bfe_u32 s8, s8, 0x3000c
	s_add_i32 s8, s6, s8
	s_and_b32 s9, s8, 0xf8
	s_sub_i32 s6, s6, s9
	s_lshl_b32 s7, s7, 3
	s_sext_i32_i8 s6, s6
	s_add_i32 s9, s7, s6
	s_bfe_i32 s6, s8, 0x80000
	s_sext_i32_i16 s6, s6
	s_ashr_i32 s7, s6, 3
	s_lshr_b32 s6, s6, 3
	v_writelane_b32 v252, s7, 35
	s_bfe_i64 s[6:7], s[6:7], 0x100000
	s_lshl_b64 s[6:7], s[6:7], 19
	v_writelane_b32 v252, s6, 36
	s_nop 1
	v_writelane_b32 v252, s7, 37
	v_writelane_b32 v252, s9, 38
	s_lshl_b32 s6, s9, 8
	v_writelane_b32 v252, s6, 39
	s_bitset1_b32 s6, 7
	s_cmp_eq_u32 s5, 0
	s_cselect_b32 s22, s3, s64
	s_lshl_b32 s3, s33, 2
	s_sub_i32 s3, s12, s3
	s_lshl_b32 s5, s64, 5
	s_sub_i32 s3, s3, s5
	v_writelane_b32 v252, s6, 40
	s_sub_i32 s0, 0, s0
	s_add_i32 s6, s3, -4
	s_ashr_i32 s3, s2, 31
	v_writelane_b32 v252, s0, 41
	s_lshl_b64 s[8:9], s[2:3], 9
	v_writelane_b32 v252, s8, 42
	s_mul_i32 s0, s64, 0x480
	s_add_i32 s0, s0, 0xfffdc060
	v_writelane_b32 v252, s9, 43
	s_lshl_b64 s[8:9], s[2:3], 8
	v_writelane_b32 v252, s8, 44
	s_mul_hi_i32 s3, s2, 0x1c00
	s_mul_i32 s2, s10, 0x7000
	v_writelane_b32 v252, s9, 45
	v_writelane_b32 v252, s10, 46
	v_writelane_b32 v252, s2, 47
	s_ashr_i32 s7, s6, 31
	s_ashr_i32 s13, s12, 31
	v_writelane_b32 v252, s3, 48
; __global__ void __launch_bounds__(512, 2) trunk_fwd(Args a_unused) {
;     ...
; #pragma unroll 1
;     for (int l = 0; l < DEPTH; ++l) {
;         const int p0 = 2 + 9 * l;
;         const bool lastl = (l == DEPTH - 1);
;         PB_BEG(2);
;         if (IN(p0 + 0)) {
;             CArgs& a = *kargs();
;             pg8::DenseSched S; S.init((const bf16*)(a.ws + WS_WIN) + (size_t)l * D_INP * 1024, 1024, NTOK, D_INP, nblk, bid, 0);
;             pg8::EpiBf16 E{(bf16*)(a.ws + WS_P), D_INP, 0};
;             pg8::gemm_phase<pg8::EpiBf16, pg8::DenseSched, true>(lds, (const char*)(a.ws + WS_HB), 1024, S, E);
;         }
;         SEAM(p0 + 0); PB_END(2); PB_BEG(3);
;         if (IN(p0 + 1)) { CArgs& a = *kargs(); PB_BEG(50); ph_prep_conv(a, l, lds, bid, nblk); PB_END(50); PB_BEG(51); ph_prep_tok(a, l, lds, ngw - 1 - gw, ngw);        PB_END(51); }
;         SEAM(p0 + 1); PB_END(3); PB_BEG(4);
;         if (IN(p0 + 2)) { CArgs& a = *kargs(); ph_scan(a, l, lds, bid, nblk, tacc); }
;         SEAM(p0 + 2); PB_END(4); PB_BEG(5);
;         if (IN(p0 + 3)) { CArgs& a = *kargs(); PB_BEG(52); ph_post_hyena(a, l, lds, bid, nblk); PB_END(52); PB_BEG(53); ph_post_tok(a, l, ngw - 1 - gw, ngw); PB_END(53); }
;         SEAM(p0 + 3); PB_END(5); PB_BEG(6);
;         if (IN(p0 + 4)) {
;             CArgs& a = *kargs();
;             const int r0 = lastl ? NTOK_C : 0;
;             pg8::DenseSched S; S.init((const bf16*)(a.ws + WS_WOUT) + (size_t)l * 1024 * 1024, 1024, NTOK - r0, 1024, nblk, bid, r0);
;             pg8::EpiBf16 E{(bf16*)(a.ws + WS_TMP), 1024, r0};
;             pg8::gemm_phase<pg8::EpiBf16, pg8::DenseSched, true>(lds, (const char*)(a.ws + WS_YMIX), 1024, S, E);
;         }
;         SEAM(p0 + 4); PB_END(6); PB_BEG(7);
;         if (IN(p0 + 5)) { CArgs& a = *kargs(); ph_ln1_route(a, l, lds, bid, nblk); }
;         SEAM(p0 + 5); PB_END(7); PB_BEG(8);
;         if (IN(p0 + 6)) {
;             CArgs& a = *kargs();
;             moe_tables(a, l, lds, 8);
;             const LAS int* tb = (const LAS int*)(lds + TAB_OFF);
;             pg8::MoeSched<true, 8> S; S.Bt = (const char*)(a.ws + WS_WGU); S.bstride = (size_t)2048 * 1024; S.rb = 1024; S.list = (const int*)(a.ws + WS_LIST);
;             S.pre = tb; S.mtl = tb + 40; S.rowoff = tb + 80; S.cnt = tb + 120; S.K = 1024; S.G = nblk; S.c = (nblk % 8 == 0) ? (bid % 8) * (nblk / 8) + bid / 8 : bid; S.total = tb[32];
	s_mul_i32 s2, s68, 0x38000
	s_mul_hi_i32 s3, s12, 0x1c00
	v_writelane_b32 v252, s2, 49
	s_ashr_i32 s37, s36, 31
	s_movk_i32 s33, 0x50
	v_writelane_b32 v252, s3, 50
	v_writelane_b32 v252, s0, 51
	s_mul_i32 s0, s64, 0x48000
	s_add_i32 s0, s0, 0xfdc06000
	v_writelane_b32 v252, s0, 52
	s_mul_i32 s0, s64, 0x24000
	s_add_i32 s0, s0, 0xfee03000
	v_writelane_b32 v252, s0, 53
	s_mul_i32 s0, s68, 24
	s_add_i32 s0, s0, -1
	v_writelane_b32 v252, s0, 54
	s_lshl_b32 s0, s1, 3
	v_writelane_b32 v252, s0, 55
	s_lshl_b32 s0, s4, 2
	v_writelane_b32 v252, s0, 56
	s_lshl_b32 s0, s68, 6
	v_writelane_b32 v252, s0, 57
	s_mul_i32 s2, s68, 36
	s_mul_i32 s0, s64, 36
	v_writelane_b32 v252, s2, 58
	v_writelane_b32 v252, s0, 59
	s_addk_i32 s0, 0xee01
	v_writelane_b32 v252, s0, 60
	s_mul_i32 s0, s64, 0x900
	s_mul_i32 s2, s68, 0x900
	v_writelane_b32 v252, s2, 61
	s_sub_i32 s2, 0x480bf, s0
	v_writelane_b32 v252, s2, 62
	v_writelane_b32 v252, s0, 63
	s_sub_i32 s0, 0x488bf, s0
	v_writelane_b32 v250, s0, 0
	v_writelane_b32 v250, s11, 1
	s_lshl_b32 s0, s11, 7
	v_writelane_b32 v250, s0, 2
	s_add_i32 s0, s14, -1
	v_writelane_b32 v250, s0, 3
	s_add_i32 s0, s12, -1
	v_writelane_b32 v250, s0, 4
	s_add_i32 s0, s36, -1
	v_writelane_b32 v250, s0, 5
	s_add_i32 s0, 0, 0xe400
	v_writelane_b32 v250, s0, 6
	s_add_i32 s0, 0, 0x10210
	v_writelane_b32 v250, s0, 7
	s_add_i32 s0, 0, 0x1c200
	v_writelane_b32 v250, s0, 8
	s_add_i32 s0, 0, 0x10100
	v_writelane_b32 v250, s0, 9
	s_add_i32 s0, 0, 0x1e200
	v_writelane_b32 v250, s0, 10
	s_add_i32 s0, 0, 0x1d200
	v_writelane_b32 v250, s0, 11
	s_add_i32 s0, 0, 0x18200
	v_writelane_b32 v250, s0, 12
	s_add_i32 s0, 0, 0x23180
	v_writelane_b32 v250, s0, 13
	s_add_i32 s0, 0, 0x2317c
	v_writelane_b32 v250, s0, 14
	v_cmp_eq_u32_e64 s[2:3], 0, v0
	s_mov_b32 s1, s22
	s_mov_b32 s0, s6
	v_writelane_b32 v250, s2, 15
	s_nop 1
	v_writelane_b32 v250, s3, 16
	s_lshl_b64 s[2:3], s[6:7], 9
	v_writelane_b32 v250, s2, 17
	s_nop 1
	v_writelane_b32 v250, s3, 18
	s_lshl_b64 s[2:3], s[12:13], 9
	v_writelane_b32 v250, s2, 19
	s_nop 1
	v_writelane_b32 v250, s3, 20
	v_writelane_b32 v250, s0, 21
	s_lshl_b64 s[2:3], s[6:7], 8
	s_nop 0
	v_writelane_b32 v250, s1, 22
	v_writelane_b32 v250, s2, 23
	s_mov_b32 s0, s12
	s_nop 0
	v_writelane_b32 v250, s3, 24
	v_writelane_b32 v250, s0, 25
	s_lshl_b64 s[2:3], s[12:13], 8
	s_mov_b64 s[12:13], 0x20000
	v_writelane_b32 v250, s1, 26
	v_writelane_b32 v250, s2, 27
	s_nop 1
	v_writelane_b32 v250, s3, 28
	s_lshl_b64 s[2:3], s[36:37], 11
	v_writelane_b32 v250, s2, 29
	s_mov_b32 s37, s1
	s_mov_b64 s[0:1], 0
	v_writelane_b32 v250, s3, 30
	v_writelane_b32 v250, s0, 31
	s_nop 1
	v_writelane_b32 v250, s1, 32
	s_mov_b64 s[0:1], 0
	v_writelane_b32 v250, s0, 33
	s_nop 1
	v_writelane_b32 v250, s1, 34
	v_writelane_b32 v250, s60, 35
	s_mov_b32 s0, s36
	s_nop 0
	v_writelane_b32 v250, s61, 36
	v_writelane_b32 v250, s0, 37
	s_nop 1
	v_writelane_b32 v250, s1, 38
	v_writelane_b32 v250, s22, 39
	v_writelane_b32 v250, s37, 40
	v_writelane_b32 v250, s69, 41
	v_writelane_b32 v250, s74, 42
	v_writelane_b32 v250, s86, 43
	s_nop 1
	v_writelane_b32 v250, s87, 44
	v_writelane_b32 v250, s88, 45
	s_nop 1
	v_writelane_b32 v250, s89, 46
	v_writelane_b32 v250, s90, 47
	s_nop 1
	v_writelane_b32 v250, s91, 48
	v_writelane_b32 v250, s92, 49
	s_nop 1
	v_writelane_b32 v250, s93, 50
	v_writelane_b32 v250, s94, 51
	s_nop 1
	v_writelane_b32 v250, s95, 52
	v_writelane_b32 v250, s96, 53
	s_nop 1
	v_writelane_b32 v250, s97, 54
	v_writelane_b32 v250, s72, 55
	s_nop 1
	v_writelane_b32 v250, s73, 56
	s_branch .LBB0_190

; #define LAS __attribute__((address_space(3)))
; __device__ __forceinline__ float bf2f(unsigned v) { return __uint_as_float(v << 16); }
; __device__ __forceinline__ unsigned f2bf(float f) { unsigned u = __float_as_uint(f); return (u + 0x7fffu + ((u >> 16) & 1u)) >> 16; }
; __device__ __forceinline__ void gla_s1(CArgs& a, int u, GlaIn& in, LAS unsigned char* ub, int w, int lane) {
;     bf16* QC = (bf16*)(a.ws + WS_CKA + CA_QC) + (size_t)u * 2048; float* DL = (float*)(a.ws + WS_CKA + CA_DL) + (size_t)u * 32;
;     LAS bf16* QE = (LAS bf16*)ub; LAS bf16* KE = QE + 2560; LAS bf16* KTT = KE + 2560; LAS bf16* VT = KTT + 2304;
;     if (w < 4) {
;         const int k = lane & 31, half = lane >> 5;
;         float run = 0.f;
; #pragma unroll
;         for (int i = 0; i < 32; ++i) { run += __uint_as_float(__float_as_uint(in.bc[i]) << 16); in.bc[i] = run; }
;         const float tot0 = __shfl(run, k), tot1 = __shfl(run, 32 + k);
;         const float bref = tot0, blast = tot0 + tot1, off = half ? tot0 : 0.f;
;         const float sc = (w == 0 || w == 2) ? 0.17677669529663687f : 1.f;
; #pragma unroll
;         for (int i = 0; i < 32; ++i) { const int t = 32 * half + i; const float bi = in.bc[i] + off;
;             const float x = bf2f(in.px[i]) * sc;
;             const float ex = w == 0 ? bi - bref : (w == 1 ? bref - bi : (w == 2 ? bi : blast - bi));
;             const bf16 y = (bf16)f2bf(x * __expf(ex));
;             if (w == 0) QE[t * 40 + k] = y; else if (w == 1) KE[t * 40 + k] = y; else if (w == 2) QC[t * 32 + k] = y; else KTT[k * 72 + t] = y; }
;         if (w == 2 && half == 0) DL[k] = __expf(blast);
;     } else {
;         const int vv = 16 * (w - 4) + (lane & 15), tq = lane >> 4;
; #pragma unroll
;         for (int i = 0; i < 16; ++i) VT[vv * 72 + 16 * tq + i] = in.px[i];
;     }
;     asm volatile("s_waitcnt lgkmcnt(0)" ::: "memory");
; }
.LBB0_372:
	s_add_i32 s36, s1, s54
	s_add_i32 s78, s36, 0xffffee00
	s_lshl_b64 s[28:29], s[78:79], 12
	s_andn2_b64 vcc, exec, s[2:3]
	v_and_b32_e32 v43, 31, v1
	s_cbranch_vccnz .LBB0_1014
	s_waitcnt vmcnt(0)
	v_lshlrev_b32_e32 v2, 16, v84
	v_lshlrev_b32_e32 v3, 16, v85
	v_add_f32_e32 v84, 0, v2
	v_add_f32_e32 v85, v84, v3
	v_lshlrev_b32_e32 v2, 16, v86
	v_lshlrev_b32_e32 v3, 16, v87
	v_add_f32_e32 v86, v85, v2
	v_add_f32_e32 v87, v86, v3
	v_lshlrev_b32_e32 v2, 16, v88
	v_lshlrev_b32_e32 v3, 16, v89
	v_add_f32_e32 v88, v87, v2
	v_add_f32_e32 v89, v88, v3
	v_lshlrev_b32_e32 v2, 16, v90
	v_lshlrev_b32_e32 v3, 16, v91
	v_add_f32_e32 v90, v89, v2
	v_add_f32_e32 v91, v90, v3
	v_lshlrev_b32_e32 v2, 16, v92
	v_lshlrev_b32_e32 v3, 16, v93
	v_add_f32_e32 v92, v91, v2
	v_add_f32_e32 v93, v92, v3
	v_lshlrev_b32_e32 v2, 16, v94
	v_lshlrev_b32_e32 v3, 16, v95
	v_add_f32_e32 v94, v93, v2
	v_add_f32_e32 v95, v94, v3
	v_lshlrev_b32_e32 v2, 16, v96
	v_lshlrev_b32_e32 v3, 16, v97
	v_add_f32_e32 v96, v95, v2
	v_add_f32_e32 v97, v96, v3
	v_lshlrev_b32_e32 v2, 16, v98
	v_lshlrev_b32_e32 v3, 16, v99
	v_add_f32_e32 v98, v97, v2
	v_add_f32_e32 v99, v98, v3
	v_lshlrev_b32_e32 v2, 16, v101
	v_lshlrev_b32_e32 v3, 16, v102
	v_add_f32_e32 v101, v99, v2
	v_add_f32_e32 v102, v101, v3
	v_lshlrev_b32_e32 v2, 16, v106
	v_lshlrev_b32_e32 v3, 16, v109
	v_add_f32_e32 v106, v102, v2
	v_add_f32_e32 v109, v106, v3
	v_lshlrev_b32_e32 v2, 16, v113
	v_lshlrev_b32_e32 v3, 16, v116
	v_add_f32_e32 v113, v109, v2
	v_add_f32_e32 v116, v113, v3
	v_lshlrev_b32_e32 v2, 16, v119
	v_lshlrev_b32_e32 v3, 16, v121
	v_add_f32_e32 v119, v116, v2
	v_add_f32_e32 v121, v119, v3
	v_lshlrev_b32_e32 v2, 16, v127
	v_lshlrev_b32_e32 v3, 16, v130
	v_add_f32_e32 v127, v121, v2
	v_add_f32_e32 v130, v127, v3
	v_lshlrev_b32_e32 v2, 16, v133
	v_lshlrev_b32_e32 v3, 16, v136
	v_add_f32_e32 v133, v130, v2
	v_add_f32_e32 v136, v133, v3
	v_lshlrev_b32_e32 v2, 16, v140
	v_lshlrev_b32_e32 v3, 16, v142
	v_add_f32_e32 v140, v136, v2
	v_add_f32_e32 v142, v140, v3
	v_lshlrev_b32_e32 v2, 16, v145
	v_lshlrev_b32_e32 v3, 16, v146
	v_add_f32_e32 v145, v142, v2
	v_and_or_b32 v2, v195, 64, v43
	v_add_f32_e32 v146, v145, v3
	v_lshlrev_b32_e32 v2, 2, v2
	ds_bpermute_b32 v4, v2, v146
	ds_bpermute_b32 v2, v2, v146 offset:128
	v_cmp_gt_u32_e64 s[48:49], 32, v1
	s_mov_b64 s[2:3], -1
	s_and_b64 vcc, exec, s[86:87]
	s_waitcnt lgkmcnt(1)
	v_cndmask_b32_e64 v6, v4, 0, s[48:49]
	s_waitcnt lgkmcnt(0)
	v_add_f32_e32 v3, v4, v2
	s_nop 0
	v_lshl_add_u32 v232, v43, 1, 0
	s_movk_i32 s2, 0x8e
	v_mad_u32_u24 v233, v43, s2, v232
	v_and_b32_e32 v234, 0xffffffe0, v1
	v_readlane_b32 s3, v249, 3
	v_mov_b32_e32 v222, 1.0
	v_mov_b32_e32 v223, 0
	v_mad_u32_u24 v224, v234, s33, v232
	v_mov_b32_e32 v225, s33
	s_cmp_lg_u32 s3, 0
	s_cbranch_scc1 .LgsA_1
	v_xor_b32_e32 v223, 0x80000000, v4
.LgsA_1:
	s_cmp_lg_u32 s3, 1
	s_cbranch_scc1 .LgsA_2
	v_mov_b32_e32 v222, -1.0
	v_mov_b32_e32 v223, v4
	v_add_u32_e32 v224, 0x1400, v224
.LgsA_2:
	s_cmp_lg_u32 s3, 3
	s_cbranch_scc1 .LgsA_3
	v_mov_b32_e32 v222, -1.0
	v_mov_b32_e32 v223, v3
	v_lshl_add_u32 v224, v234, 1, v233
	v_add_u32_e32 v224, 0x2800, v224
	v_mov_b32_e32 v225, 2
.LgsA_3:
	s_cmp_eq_u32 s3, 2
	s_cbranch_scc1 .LgsA_qc
	v_add_f32_e32 v226, v84, v6
	v_add_f32_e32 v228, v85, v6
	v_fma_f32 v226, v226, v222, v223
	v_fma_f32 v228, v228, v222, v223
	v_mul_f32_e32 v226, 0x3fb8aa3b, v226
	v_mul_f32_e32 v228, 0x3fb8aa3b, v228
	v_exp_f32_e32 v226, v226
	v_exp_f32_e32 v228, v228
	v_lshlrev_b32_e32 v227, 16, v103
	v_lshlrev_b32_e32 v229, 16, v105
	v_mul_f32_e32 v227, v124, v227
	v_mul_f32_e32 v229, v124, v229
	v_mul_f32_e32 v226, v227, v226
	v_mul_f32_e32 v228, v229, v228
	v_cvt_pk_bf16_f32 v226, v226, v226
	v_cvt_pk_bf16_f32 v228, v228, v228
	ds_write_b16 v224, v226
	v_add_u32_e32 v224, v225, v224
	ds_write_b16 v224, v228
	v_add_u32_e32 v224, v225, v224
	v_add_f32_e32 v226, v86, v6
	v_add_f32_e32 v228, v87, v6
	v_fma_f32 v226, v226, v222, v223
	v_fma_f32 v228, v228, v222, v223
	v_mul_f32_e32 v226, 0x3fb8aa3b, v226
	v_mul_f32_e32 v228, 0x3fb8aa3b, v228
	v_exp_f32_e32 v226, v226
	v_exp_f32_e32 v228, v228
	v_lshlrev_b32_e32 v227, 16, v108
	v_lshlrev_b32_e32 v229, 16, v110
	v_mul_f32_e32 v227, v124, v227
	v_mul_f32_e32 v229, v124, v229
	v_mul_f32_e32 v226, v227, v226
	v_mul_f32_e32 v228, v229, v228
	v_cvt_pk_bf16_f32 v226, v226, v226
	v_cvt_pk_bf16_f32 v228, v228, v228
	ds_write_b16 v224, v226
	v_add_u32_e32 v224, v225, v224
	ds_write_b16 v224, v228
	v_add_u32_e32 v224, v225, v224
	v_add_f32_e32 v226, v88, v6
	v_add_f32_e32 v228, v89, v6
	v_fma_f32 v226, v226, v222, v223
	v_fma_f32 v228, v228, v222, v223
	v_mul_f32_e32 v226, 0x3fb8aa3b, v226
	v_mul_f32_e32 v228, 0x3fb8aa3b, v228
	v_exp_f32_e32 v226, v226
	v_exp_f32_e32 v228, v228
	v_lshlrev_b32_e32 v227, 16, v112
	v_lshlrev_b32_e32 v229, 16, v115
	v_mul_f32_e32 v227, v124, v227
	v_mul_f32_e32 v229, v124, v229
	v_mul_f32_e32 v226, v227, v226
	v_mul_f32_e32 v228, v229, v228
	v_cvt_pk_bf16_f32 v226, v226, v226
	v_cvt_pk_bf16_f32 v228, v228, v228
	ds_write_b16 v224, v226
	v_add_u32_e32 v224, v225, v224
	ds_write_b16 v224, v228
	v_add_u32_e32 v224, v225, v224
	v_add_f32_e32 v226, v90, v6
	v_add_f32_e32 v228, v91, v6
	v_fma_f32 v226, v226, v222, v223
	v_fma_f32 v228, v228, v222, v223
	v_mul_f32_e32 v226, 0x3fb8aa3b, v226
	v_mul_f32_e32 v228, 0x3fb8aa3b, v228
	v_exp_f32_e32 v226, v226
	v_exp_f32_e32 v228, v228
	v_lshlrev_b32_e32 v227, 16, v117
	v_lshlrev_b32_e32 v229, 16, v122
	v_mul_f32_e32 v227, v124, v227
	v_mul_f32_e32 v229, v124, v229
	v_mul_f32_e32 v226, v227, v226
	v_mul_f32_e32 v228, v229, v228
	v_cvt_pk_bf16_f32 v226, v226, v226
	v_cvt_pk_bf16_f32 v228, v228, v228
; __device__ __forceinline__ float bf2f(unsigned v) { return __uint_as_float(v << 16); }
; __device__ __forceinline__ unsigned f2bf(float f) { unsigned u = __float_as_uint(f); return (u + 0x7fffu + ((u >> 16) & 1u)) >> 16; }
; __device__ __forceinline__ void gla_s1(CArgs& a, int u, GlaIn& in, LAS unsigned char* ub, int w, int lane) {
;     ...
;         for (int i = 0; i < 32; ++i) { const int t = 32 * half + i; const float bi = in.bc[i] + off;
;             const float x = bf2f(in.px[i]) * sc;
;             const float ex = w == 0 ? bi - bref : (w == 1 ? bref - bi : (w == 2 ? bi : blast - bi));
;             const bf16 y = (bf16)f2bf(x * __expf(ex));
;             if (w == 0) QE[t * 40 + k] = y; else if (w == 1) KE[t * 40 + k] = y; else if (w == 2) QC[t * 32 + k] = y; else KTT[k * 72 + t] = y; }
	ds_write_b16 v224, v226
	v_add_u32_e32 v224, v225, v224
	ds_write_b16 v224, v228
	v_add_u32_e32 v224, v225, v224
	v_add_f32_e32 v226, v92, v6
	v_add_f32_e32 v228, v93, v6
	v_fma_f32 v226, v226, v222, v223
	v_fma_f32 v228, v228, v222, v223
	v_mul_f32_e32 v226, 0x3fb8aa3b, v226
	v_mul_f32_e32 v228, 0x3fb8aa3b, v228
	v_exp_f32_e32 v226, v226
	v_exp_f32_e32 v228, v228
	v_lshlrev_b32_e32 v227, 16, v123
	v_lshlrev_b32_e32 v229, 16, v126
	v_mul_f32_e32 v227, v124, v227
	v_mul_f32_e32 v229, v124, v229
	v_mul_f32_e32 v226, v227, v226
	v_mul_f32_e32 v228, v229, v228
	v_cvt_pk_bf16_f32 v226, v226, v226
	v_cvt_pk_bf16_f32 v228, v228, v228
	ds_write_b16 v224, v226
	v_add_u32_e32 v224, v225, v224
	ds_write_b16 v224, v228
	v_add_u32_e32 v224, v225, v224
	v_add_f32_e32 v226, v94, v6
	v_add_f32_e32 v228, v95, v6
	v_fma_f32 v226, v226, v222, v223
	v_fma_f32 v228, v228, v222, v223
	v_mul_f32_e32 v226, 0x3fb8aa3b, v226
	v_mul_f32_e32 v228, 0x3fb8aa3b, v228
	v_exp_f32_e32 v226, v226
	v_exp_f32_e32 v228, v228
	v_lshlrev_b32_e32 v227, 16, v129
	v_lshlrev_b32_e32 v229, 16, v132
	v_mul_f32_e32 v227, v124, v227
	v_mul_f32_e32 v229, v124, v229
	v_mul_f32_e32 v226, v227, v226
	v_mul_f32_e32 v228, v229, v228
	v_cvt_pk_bf16_f32 v226, v226, v226
	v_cvt_pk_bf16_f32 v228, v228, v228
	ds_write_b16 v224, v226
	v_add_u32_e32 v224, v225, v224
	ds_write_b16 v224, v228
	v_add_u32_e32 v224, v225, v224
	v_add_f32_e32 v226, v96, v6
	v_add_f32_e32 v228, v97, v6
	v_fma_f32 v226, v226, v222, v223
	v_fma_f32 v228, v228, v222, v223
	v_mul_f32_e32 v226, 0x3fb8aa3b, v226
	v_mul_f32_e32 v228, 0x3fb8aa3b, v228
	v_exp_f32_e32 v226, v226
	v_exp_f32_e32 v228, v228
	v_lshlrev_b32_e32 v227, 16, v135
	v_lshlrev_b32_e32 v229, 16, v137
	v_mul_f32_e32 v227, v124, v227
	v_mul_f32_e32 v229, v124, v229
	v_mul_f32_e32 v226, v227, v226
	v_mul_f32_e32 v228, v229, v228
	v_cvt_pk_bf16_f32 v226, v226, v226
	v_cvt_pk_bf16_f32 v228, v228, v228
	ds_write_b16 v224, v226
	v_add_u32_e32 v224, v225, v224
	ds_write_b16 v224, v228
	v_add_u32_e32 v224, v225, v224
	v_add_f32_e32 v226, v98, v6
	v_add_f32_e32 v228, v99, v6
	v_fma_f32 v226, v226, v222, v223
	v_fma_f32 v228, v228, v222, v223
	v_mul_f32_e32 v226, 0x3fb8aa3b, v226
	v_mul_f32_e32 v228, 0x3fb8aa3b, v228
	v_exp_f32_e32 v226, v226
	v_exp_f32_e32 v228, v228
	v_lshlrev_b32_e32 v227, 16, v138
	v_lshlrev_b32_e32 v229, 16, v143
	v_mul_f32_e32 v227, v124, v227
	v_mul_f32_e32 v229, v124, v229
	v_mul_f32_e32 v226, v227, v226
	v_mul_f32_e32 v228, v229, v228
	v_cvt_pk_bf16_f32 v226, v226, v226
	v_cvt_pk_bf16_f32 v228, v228, v228
	ds_write_b16 v224, v226
	v_add_u32_e32 v224, v225, v224
	ds_write_b16 v224, v228
	v_add_u32_e32 v224, v225, v224
	v_add_f32_e32 v226, v101, v6
	v_add_f32_e32 v228, v102, v6
	v_fma_f32 v226, v226, v222, v223
	v_fma_f32 v228, v228, v222, v223
	v_mul_f32_e32 v226, 0x3fb8aa3b, v226
	v_mul_f32_e32 v228, 0x3fb8aa3b, v228
	v_exp_f32_e32 v226, v226
	v_exp_f32_e32 v228, v228
	v_lshlrev_b32_e32 v227, 16, v100
	v_lshlrev_b32_e32 v229, 16, v104
	v_mul_f32_e32 v227, v124, v227
	v_mul_f32_e32 v229, v124, v229
	v_mul_f32_e32 v226, v227, v226
	v_mul_f32_e32 v228, v229, v228
	v_cvt_pk_bf16_f32 v226, v226, v226
	v_cvt_pk_bf16_f32 v228, v228, v228
	ds_write_b16 v224, v226
	v_add_u32_e32 v224, v225, v224
	ds_write_b16 v224, v228
	v_add_u32_e32 v224, v225, v224
	v_add_f32_e32 v226, v106, v6
	v_add_f32_e32 v228, v109, v6
	v_fma_f32 v226, v226, v222, v223
	v_fma_f32 v228, v228, v222, v223
	v_mul_f32_e32 v226, 0x3fb8aa3b, v226
	v_mul_f32_e32 v228, 0x3fb8aa3b, v228
	v_exp_f32_e32 v226, v226
	v_exp_f32_e32 v228, v228
	v_lshlrev_b32_e32 v227, 16, v107
	v_lshlrev_b32_e32 v229, 16, v111
	v_mul_f32_e32 v227, v124, v227
	v_mul_f32_e32 v229, v124, v229
	v_mul_f32_e32 v226, v227, v226
	v_mul_f32_e32 v228, v229, v228
	v_cvt_pk_bf16_f32 v226, v226, v226
	v_cvt_pk_bf16_f32 v228, v228, v228
	ds_write_b16 v224, v226
	v_add_u32_e32 v224, v225, v224
	ds_write_b16 v224, v228
	v_add_u32_e32 v224, v225, v224
	v_add_f32_e32 v226, v113, v6
	v_add_f32_e32 v228, v116, v6
	v_fma_f32 v226, v226, v222, v223
	v_fma_f32 v228, v228, v222, v223
	v_mul_f32_e32 v226, 0x3fb8aa3b, v226
	v_mul_f32_e32 v228, 0x3fb8aa3b, v228
	v_exp_f32_e32 v226, v226
	v_exp_f32_e32 v228, v228
	v_lshlrev_b32_e32 v227, 16, v114
	v_lshlrev_b32_e32 v229, 16, v118
	v_mul_f32_e32 v227, v124, v227
	v_mul_f32_e32 v229, v124, v229
	v_mul_f32_e32 v226, v227, v226
	v_mul_f32_e32 v228, v229, v228
	v_cvt_pk_bf16_f32 v226, v226, v226
	v_cvt_pk_bf16_f32 v228, v228, v228
	ds_write_b16 v224, v226
	v_add_u32_e32 v224, v225, v224
	ds_write_b16 v224, v228
	v_add_u32_e32 v224, v225, v224
	v_add_f32_e32 v226, v119, v6
	v_add_f32_e32 v228, v121, v6
	v_fma_f32 v226, v226, v222, v223
	v_fma_f32 v228, v228, v222, v223
	v_mul_f32_e32 v226, 0x3fb8aa3b, v226
	v_mul_f32_e32 v228, 0x3fb8aa3b, v228
	v_exp_f32_e32 v226, v226
	v_exp_f32_e32 v228, v228
	v_lshlrev_b32_e32 v227, 16, v120
	v_lshlrev_b32_e32 v229, 16, v125
	v_mul_f32_e32 v227, v124, v227
	v_mul_f32_e32 v229, v124, v229
	v_mul_f32_e32 v226, v227, v226
	v_mul_f32_e32 v228, v229, v228
	v_cvt_pk_bf16_f32 v226, v226, v226
	v_cvt_pk_bf16_f32 v228, v228, v228
	ds_write_b16 v224, v226
	v_add_u32_e32 v224, v225, v224
	ds_write_b16 v224, v228
	v_add_u32_e32 v224, v225, v224
	v_add_f32_e32 v226, v127, v6
	v_add_f32_e32 v228, v130, v6
	v_fma_f32 v226, v226, v222, v223
	v_fma_f32 v228, v228, v222, v223
	v_mul_f32_e32 v226, 0x3fb8aa3b, v226
	v_mul_f32_e32 v228, 0x3fb8aa3b, v228
	v_exp_f32_e32 v226, v226
	v_exp_f32_e32 v228, v228
	v_lshlrev_b32_e32 v227, 16, v128
	v_lshlrev_b32_e32 v229, 16, v131
	v_mul_f32_e32 v227, v124, v227
	v_mul_f32_e32 v229, v124, v229
	v_mul_f32_e32 v226, v227, v226
; __device__ __forceinline__ float bf2f(unsigned v) { return __uint_as_float(v << 16); }
; __device__ __forceinline__ unsigned f2bf(float f) { unsigned u = __float_as_uint(f); return (u + 0x7fffu + ((u >> 16) & 1u)) >> 16; }
; __device__ __forceinline__ void gla_s1(CArgs& a, int u, GlaIn& in, LAS unsigned char* ub, int w, int lane) {
;     ...
;         for (int i = 0; i < 32; ++i) { const int t = 32 * half + i; const float bi = in.bc[i] + off;
;             const float x = bf2f(in.px[i]) * sc;
;             const float ex = w == 0 ? bi - bref : (w == 1 ? bref - bi : (w == 2 ? bi : blast - bi));
;             const bf16 y = (bf16)f2bf(x * __expf(ex));
;             if (w == 0) QE[t * 40 + k] = y; else if (w == 1) KE[t * 40 + k] = y; else if (w == 2) QC[t * 32 + k] = y; else KTT[k * 72 + t] = y; }
;         if (w == 2 && half == 0) DL[k] = __expf(blast);
	v_mul_f32_e32 v228, v229, v228
	v_cvt_pk_bf16_f32 v226, v226, v226
	v_cvt_pk_bf16_f32 v228, v228, v228
	ds_write_b16 v224, v226
	v_add_u32_e32 v224, v225, v224
	ds_write_b16 v224, v228
	v_add_u32_e32 v224, v225, v224
	v_add_f32_e32 v226, v133, v6
	v_add_f32_e32 v228, v136, v6
	v_fma_f32 v226, v226, v222, v223
	v_fma_f32 v228, v228, v222, v223
	v_mul_f32_e32 v226, 0x3fb8aa3b, v226
	v_mul_f32_e32 v228, 0x3fb8aa3b, v228
	v_exp_f32_e32 v226, v226
	v_exp_f32_e32 v228, v228
	v_lshlrev_b32_e32 v227, 16, v134
	v_lshlrev_b32_e32 v229, 16, v139
	v_mul_f32_e32 v227, v124, v227
	v_mul_f32_e32 v229, v124, v229
	v_mul_f32_e32 v226, v227, v226
	v_mul_f32_e32 v228, v229, v228
	v_cvt_pk_bf16_f32 v226, v226, v226
	v_cvt_pk_bf16_f32 v228, v228, v228
	ds_write_b16 v224, v226
	v_add_u32_e32 v224, v225, v224
	ds_write_b16 v224, v228
	v_add_u32_e32 v224, v225, v224
	v_add_f32_e32 v226, v140, v6
	v_add_f32_e32 v228, v142, v6
	v_fma_f32 v226, v226, v222, v223
	v_fma_f32 v228, v228, v222, v223
	v_mul_f32_e32 v226, 0x3fb8aa3b, v226
	v_mul_f32_e32 v228, 0x3fb8aa3b, v228
	v_exp_f32_e32 v226, v226
	v_exp_f32_e32 v228, v228
	v_lshlrev_b32_e32 v227, 16, v141
	v_lshlrev_b32_e32 v229, 16, v144
	v_mul_f32_e32 v227, v124, v227
	v_mul_f32_e32 v229, v124, v229
	v_mul_f32_e32 v226, v227, v226
	v_mul_f32_e32 v228, v229, v228
	v_cvt_pk_bf16_f32 v226, v226, v226
	v_cvt_pk_bf16_f32 v228, v228, v228
	ds_write_b16 v224, v226
	v_add_u32_e32 v224, v225, v224
	ds_write_b16 v224, v228
	v_add_u32_e32 v224, v225, v224
	v_add_f32_e32 v226, v145, v6
	v_add_f32_e32 v228, v146, v6
	v_fma_f32 v226, v226, v222, v223
	v_fma_f32 v228, v228, v222, v223
	v_mul_f32_e32 v226, 0x3fb8aa3b, v226
	v_mul_f32_e32 v228, 0x3fb8aa3b, v228
	v_exp_f32_e32 v226, v226
	v_exp_f32_e32 v228, v228
	v_lshlrev_b32_e32 v227, 16, v147
	v_lshlrev_b32_e32 v229, 16, v148
	v_mul_f32_e32 v227, v124, v227
	v_mul_f32_e32 v229, v124, v229
	v_mul_f32_e32 v226, v227, v226
	v_mul_f32_e32 v228, v229, v228
	v_cvt_pk_bf16_f32 v226, v226, v226
	v_cvt_pk_bf16_f32 v228, v228, v228
	ds_write_b16 v224, v226
	v_add_u32_e32 v224, v225, v224
	ds_write_b16 v224, v228
	v_add_u32_e32 v224, v225, v224
	s_branch .LgsA_end
.LgsA_qc:
	v_readlane_b32 s2, v249, 22
	v_readlane_b32 s3, v249, 23
	s_add_u32 s2, s2, s28
	s_addc_u32 s3, s3, s29
	v_lshl_or_b32 v230, v234, 5, v43
	v_mov_b32_e32 v231, 0
	v_lshl_add_u64 v[230:231], v[230:231], 1, s[2:3]
	v_add_f32_e32 v226, v84, v6
	v_add_f32_e32 v228, v85, v6
	v_fma_f32 v226, v226, v222, v223
	v_fma_f32 v228, v228, v222, v223
	v_mul_f32_e32 v226, 0x3fb8aa3b, v226
	v_mul_f32_e32 v228, 0x3fb8aa3b, v228
	v_exp_f32_e32 v226, v226
	v_exp_f32_e32 v228, v228
	v_lshlrev_b32_e32 v227, 16, v103
	v_lshlrev_b32_e32 v229, 16, v105
	v_mul_f32_e32 v227, v124, v227
	v_mul_f32_e32 v229, v124, v229
	v_mul_f32_e32 v226, v227, v226
	v_mul_f32_e32 v228, v229, v228
	v_cvt_pk_bf16_f32 v226, v226, v226
	v_cvt_pk_bf16_f32 v228, v228, v228
	global_store_short v[230:231], v226, off
	global_store_short v[230:231], v228, off offset:64
	v_add_f32_e32 v226, v86, v6
	v_add_f32_e32 v228, v87, v6
	v_fma_f32 v226, v226, v222, v223
	v_fma_f32 v228, v228, v222, v223
	v_mul_f32_e32 v226, 0x3fb8aa3b, v226
	v_mul_f32_e32 v228, 0x3fb8aa3b, v228
	v_exp_f32_e32 v226, v226
	v_exp_f32_e32 v228, v228
	v_lshlrev_b32_e32 v227, 16, v108
	v_lshlrev_b32_e32 v229, 16, v110
	v_mul_f32_e32 v227, v124, v227
	v_mul_f32_e32 v229, v124, v229
	v_mul_f32_e32 v226, v227, v226
	v_mul_f32_e32 v228, v229, v228
	v_cvt_pk_bf16_f32 v226, v226, v226
	v_cvt_pk_bf16_f32 v228, v228, v228
	global_store_short v[230:231], v226, off offset:128
	global_store_short v[230:231], v228, off offset:192
	v_add_f32_e32 v226, v88, v6
	v_add_f32_e32 v228, v89, v6
	v_fma_f32 v226, v226, v222, v223
	v_fma_f32 v228, v228, v222, v223
	v_mul_f32_e32 v226, 0x3fb8aa3b, v226
	v_mul_f32_e32 v228, 0x3fb8aa3b, v228
	v_exp_f32_e32 v226, v226
	v_exp_f32_e32 v228, v228
	v_lshlrev_b32_e32 v227, 16, v112
	v_lshlrev_b32_e32 v229, 16, v115
	v_mul_f32_e32 v227, v124, v227
	v_mul_f32_e32 v229, v124, v229
	v_mul_f32_e32 v226, v227, v226
	v_mul_f32_e32 v228, v229, v228
	v_cvt_pk_bf16_f32 v226, v226, v226
	v_cvt_pk_bf16_f32 v228, v228, v228
	global_store_short v[230:231], v226, off offset:256
	global_store_short v[230:231], v228, off offset:320
	v_add_f32_e32 v226, v90, v6
	v_add_f32_e32 v228, v91, v6
	v_fma_f32 v226, v226, v222, v223
	v_fma_f32 v228, v228, v222, v223
	v_mul_f32_e32 v226, 0x3fb8aa3b, v226
	v_mul_f32_e32 v228, 0x3fb8aa3b, v228
	v_exp_f32_e32 v226, v226
	v_exp_f32_e32 v228, v228
	v_lshlrev_b32_e32 v227, 16, v117
	v_lshlrev_b32_e32 v229, 16, v122
	v_mul_f32_e32 v227, v124, v227
	v_mul_f32_e32 v229, v124, v229
	v_mul_f32_e32 v226, v227, v226
	v_mul_f32_e32 v228, v229, v228
	v_cvt_pk_bf16_f32 v226, v226, v226
	v_cvt_pk_bf16_f32 v228, v228, v228
	global_store_short v[230:231], v226, off offset:384
	global_store_short v[230:231], v228, off offset:448
	v_add_f32_e32 v226, v92, v6
	v_add_f32_e32 v228, v93, v6
	v_fma_f32 v226, v226, v222, v223
	v_fma_f32 v228, v228, v222, v223
	v_mul_f32_e32 v226, 0x3fb8aa3b, v226
	v_mul_f32_e32 v228, 0x3fb8aa3b, v228
	v_exp_f32_e32 v226, v226
	v_exp_f32_e32 v228, v228
	v_lshlrev_b32_e32 v227, 16, v123
	v_lshlrev_b32_e32 v229, 16, v126
	v_mul_f32_e32 v227, v124, v227
	v_mul_f32_e32 v229, v124, v229
	v_mul_f32_e32 v226, v227, v226
	v_mul_f32_e32 v228, v229, v228
	v_cvt_pk_bf16_f32 v226, v226, v226
	v_cvt_pk_bf16_f32 v228, v228, v228
	global_store_short v[230:231], v226, off offset:512
	global_store_short v[230:231], v228, off offset:576
	v_add_f32_e32 v226, v94, v6
	v_add_f32_e32 v228, v95, v6
	v_fma_f32 v226, v226, v222, v223
	v_fma_f32 v228, v228, v222, v223
; __device__ __forceinline__ float bf2f(unsigned v) { return __uint_as_float(v << 16); }
; __device__ __forceinline__ unsigned f2bf(float f) { unsigned u = __float_as_uint(f); return (u + 0x7fffu + ((u >> 16) & 1u)) >> 16; }
; __device__ __forceinline__ void gla_s1(CArgs& a, int u, GlaIn& in, LAS unsigned char* ub, int w, int lane) {
;     ...
;         for (int i = 0; i < 32; ++i) { const int t = 32 * half + i; const float bi = in.bc[i] + off;
;             const float x = bf2f(in.px[i]) * sc;
;             const float ex = w == 0 ? bi - bref : (w == 1 ? bref - bi : (w == 2 ? bi : blast - bi));
;             const bf16 y = (bf16)f2bf(x * __expf(ex));
;             if (w == 0) QE[t * 40 + k] = y; else if (w == 1) KE[t * 40 + k] = y; else if (w == 2) QC[t * 32 + k] = y; else KTT[k * 72 + t] = y; }
;         if (w == 2 && half == 0) DL[k] = __expf(blast);
	v_mul_f32_e32 v226, 0x3fb8aa3b, v226
	v_mul_f32_e32 v228, 0x3fb8aa3b, v228
	v_exp_f32_e32 v226, v226
	v_exp_f32_e32 v228, v228
	v_lshlrev_b32_e32 v227, 16, v129
	v_lshlrev_b32_e32 v229, 16, v132
	v_mul_f32_e32 v227, v124, v227
	v_mul_f32_e32 v229, v124, v229
	v_mul_f32_e32 v226, v227, v226
	v_mul_f32_e32 v228, v229, v228
	v_cvt_pk_bf16_f32 v226, v226, v226
	v_cvt_pk_bf16_f32 v228, v228, v228
	global_store_short v[230:231], v226, off offset:640
	global_store_short v[230:231], v228, off offset:704
	v_add_f32_e32 v226, v96, v6
	v_add_f32_e32 v228, v97, v6
	v_fma_f32 v226, v226, v222, v223
	v_fma_f32 v228, v228, v222, v223
	v_mul_f32_e32 v226, 0x3fb8aa3b, v226
	v_mul_f32_e32 v228, 0x3fb8aa3b, v228
	v_exp_f32_e32 v226, v226
	v_exp_f32_e32 v228, v228
	v_lshlrev_b32_e32 v227, 16, v135
	v_lshlrev_b32_e32 v229, 16, v137
	v_mul_f32_e32 v227, v124, v227
	v_mul_f32_e32 v229, v124, v229
	v_mul_f32_e32 v226, v227, v226
	v_mul_f32_e32 v228, v229, v228
	v_cvt_pk_bf16_f32 v226, v226, v226
	v_cvt_pk_bf16_f32 v228, v228, v228
	global_store_short v[230:231], v226, off offset:768
	global_store_short v[230:231], v228, off offset:832
	v_add_f32_e32 v226, v98, v6
	v_add_f32_e32 v228, v99, v6
	v_fma_f32 v226, v226, v222, v223
	v_fma_f32 v228, v228, v222, v223
	v_mul_f32_e32 v226, 0x3fb8aa3b, v226
	v_mul_f32_e32 v228, 0x3fb8aa3b, v228
	v_exp_f32_e32 v226, v226
	v_exp_f32_e32 v228, v228
	v_lshlrev_b32_e32 v227, 16, v138
	v_lshlrev_b32_e32 v229, 16, v143
	v_mul_f32_e32 v227, v124, v227
	v_mul_f32_e32 v229, v124, v229
	v_mul_f32_e32 v226, v227, v226
	v_mul_f32_e32 v228, v229, v228
	v_cvt_pk_bf16_f32 v226, v226, v226
	v_cvt_pk_bf16_f32 v228, v228, v228
	global_store_short v[230:231], v226, off offset:896
	global_store_short v[230:231], v228, off offset:960
	v_add_f32_e32 v226, v101, v6
	v_add_f32_e32 v228, v102, v6
	v_fma_f32 v226, v226, v222, v223
	v_fma_f32 v228, v228, v222, v223
	v_mul_f32_e32 v226, 0x3fb8aa3b, v226
	v_mul_f32_e32 v228, 0x3fb8aa3b, v228
	v_exp_f32_e32 v226, v226
	v_exp_f32_e32 v228, v228
	v_lshlrev_b32_e32 v227, 16, v100
	v_lshlrev_b32_e32 v229, 16, v104
	v_mul_f32_e32 v227, v124, v227
	v_mul_f32_e32 v229, v124, v229
	v_mul_f32_e32 v226, v227, v226
	v_mul_f32_e32 v228, v229, v228
	v_cvt_pk_bf16_f32 v226, v226, v226
	v_cvt_pk_bf16_f32 v228, v228, v228
	global_store_short v[230:231], v226, off offset:1024
	global_store_short v[230:231], v228, off offset:1088
	v_add_f32_e32 v226, v106, v6
	v_add_f32_e32 v228, v109, v6
	v_fma_f32 v226, v226, v222, v223
	v_fma_f32 v228, v228, v222, v223
	v_mul_f32_e32 v226, 0x3fb8aa3b, v226
	v_mul_f32_e32 v228, 0x3fb8aa3b, v228
	v_exp_f32_e32 v226, v226
	v_exp_f32_e32 v228, v228
	v_lshlrev_b32_e32 v227, 16, v107
	v_lshlrev_b32_e32 v229, 16, v111
	v_mul_f32_e32 v227, v124, v227
	v_mul_f32_e32 v229, v124, v229
	v_mul_f32_e32 v226, v227, v226
	v_mul_f32_e32 v228, v229, v228
	v_cvt_pk_bf16_f32 v226, v226, v226
	v_cvt_pk_bf16_f32 v228, v228, v228
	global_store_short v[230:231], v226, off offset:1152
	global_store_short v[230:231], v228, off offset:1216
	v_add_f32_e32 v226, v113, v6
	v_add_f32_e32 v228, v116, v6
	v_fma_f32 v226, v226, v222, v223
	v_fma_f32 v228, v228, v222, v223
	v_mul_f32_e32 v226, 0x3fb8aa3b, v226
	v_mul_f32_e32 v228, 0x3fb8aa3b, v228
	v_exp_f32_e32 v226, v226
	v_exp_f32_e32 v228, v228
	v_lshlrev_b32_e32 v227, 16, v114
	v_lshlrev_b32_e32 v229, 16, v118
	v_mul_f32_e32 v227, v124, v227
	v_mul_f32_e32 v229, v124, v229
	v_mul_f32_e32 v226, v227, v226
	v_mul_f32_e32 v228, v229, v228
	v_cvt_pk_bf16_f32 v226, v226, v226
	v_cvt_pk_bf16_f32 v228, v228, v228
	global_store_short v[230:231], v226, off offset:1280
	global_store_short v[230:231], v228, off offset:1344
	v_add_f32_e32 v226, v119, v6
	v_add_f32_e32 v228, v121, v6
	v_fma_f32 v226, v226, v222, v223
	v_fma_f32 v228, v228, v222, v223
	v_mul_f32_e32 v226, 0x3fb8aa3b, v226
	v_mul_f32_e32 v228, 0x3fb8aa3b, v228
	v_exp_f32_e32 v226, v226
	v_exp_f32_e32 v228, v228
	v_lshlrev_b32_e32 v227, 16, v120
	v_lshlrev_b32_e32 v229, 16, v125
	v_mul_f32_e32 v227, v124, v227
	v_mul_f32_e32 v229, v124, v229
	v_mul_f32_e32 v226, v227, v226
	v_mul_f32_e32 v228, v229, v228
	v_cvt_pk_bf16_f32 v226, v226, v226
	v_cvt_pk_bf16_f32 v228, v228, v228
	global_store_short v[230:231], v226, off offset:1408
	global_store_short v[230:231], v228, off offset:1472
	v_add_f32_e32 v226, v127, v6
	v_add_f32_e32 v228, v130, v6
	v_fma_f32 v226, v226, v222, v223
	v_fma_f32 v228, v228, v222, v223
	v_mul_f32_e32 v226, 0x3fb8aa3b, v226
	v_mul_f32_e32 v228, 0x3fb8aa3b, v228
	v_exp_f32_e32 v226, v226
	v_exp_f32_e32 v228, v228
	v_lshlrev_b32_e32 v227, 16, v128
	v_lshlrev_b32_e32 v229, 16, v131
	v_mul_f32_e32 v227, v124, v227
	v_mul_f32_e32 v229, v124, v229
	v_mul_f32_e32 v226, v227, v226
	v_mul_f32_e32 v228, v229, v228
	v_cvt_pk_bf16_f32 v226, v226, v226
	v_cvt_pk_bf16_f32 v228, v228, v228
	global_store_short v[230:231], v226, off offset:1536
	global_store_short v[230:231], v228, off offset:1600
	v_add_f32_e32 v226, v133, v6
	v_add_f32_e32 v228, v136, v6
	v_fma_f32 v226, v226, v222, v223
	v_fma_f32 v228, v228, v222, v223
	v_mul_f32_e32 v226, 0x3fb8aa3b, v226
	v_mul_f32_e32 v228, 0x3fb8aa3b, v228
	v_exp_f32_e32 v226, v226
	v_exp_f32_e32 v228, v228
	v_lshlrev_b32_e32 v227, 16, v134
	v_lshlrev_b32_e32 v229, 16, v139
	v_mul_f32_e32 v227, v124, v227
	v_mul_f32_e32 v229, v124, v229
	v_mul_f32_e32 v226, v227, v226
	v_mul_f32_e32 v228, v229, v228
	v_cvt_pk_bf16_f32 v226, v226, v226
	v_cvt_pk_bf16_f32 v228, v228, v228
	global_store_short v[230:231], v226, off offset:1664
	global_store_short v[230:231], v228, off offset:1728
	v_add_f32_e32 v226, v140, v6
	v_add_f32_e32 v228, v142, v6
	v_fma_f32 v226, v226, v222, v223
	v_fma_f32 v228, v228, v222, v223
	v_mul_f32_e32 v226, 0x3fb8aa3b, v226
	v_mul_f32_e32 v228, 0x3fb8aa3b, v228
	v_exp_f32_e32 v226, v226
	v_exp_f32_e32 v228, v228
	v_lshlrev_b32_e32 v227, 16, v141
	v_lshlrev_b32_e32 v229, 16, v144
	v_mul_f32_e32 v227, v124, v227
	v_mul_f32_e32 v229, v124, v229
	v_mul_f32_e32 v226, v227, v226
	v_mul_f32_e32 v228, v229, v228
	v_cvt_pk_bf16_f32 v226, v226, v226
	v_cvt_pk_bf16_f32 v228, v228, v228
	global_store_short v[230:231], v226, off offset:1792
	global_store_short v[230:231], v228, off offset:1856
	v_add_f32_e32 v226, v145, v6
	v_add_f32_e32 v228, v146, v6
	v_fma_f32 v226, v226, v222, v223
	v_fma_f32 v228, v228, v222, v223
	v_mul_f32_e32 v226, 0x3fb8aa3b, v226
	v_mul_f32_e32 v228, 0x3fb8aa3b, v228
	v_exp_f32_e32 v226, v226
	v_exp_f32_e32 v228, v228
	v_lshlrev_b32_e32 v227, 16, v147
	v_lshlrev_b32_e32 v229, 16, v148
	v_mul_f32_e32 v227, v124, v227
	v_mul_f32_e32 v229, v124, v229
	v_mul_f32_e32 v226, v227, v226
	v_mul_f32_e32 v228, v229, v228
	v_cvt_pk_bf16_f32 v226, v226, v226
	v_cvt_pk_bf16_f32 v228, v228, v228
	global_store_short v[230:231], v226, off offset:1920
	global_store_short v[230:231], v228, off offset:1984
.LgsA_end:
.LBB0_1011:
	s_and_b64 s[26:27], s[40:41], s[48:49]
	s_and_saveexec_b64 s[2:3], s[26:27]
	s_cbranch_execz .LBB0_1013

; #define LAS __attribute__((address_space(3)))
; __device__ __forceinline__ float bf2f(unsigned v) { return __uint_as_float(v << 16); }
; __device__ __forceinline__ unsigned f2bf(float f) { unsigned u = __float_as_uint(f); return (u + 0x7fffu + ((u >> 16) & 1u)) >> 16; }
; __device__ __forceinline__ void gla_s1(CArgs& a, int u, GlaIn& in, LAS unsigned char* ub, int w, int lane) {
;     bf16* QC = (bf16*)(a.ws + WS_CKA + CA_QC) + (size_t)u * 2048; float* DL = (float*)(a.ws + WS_CKA + CA_DL) + (size_t)u * 32;
;     LAS bf16* QE = (LAS bf16*)ub; LAS bf16* KE = QE + 2560; LAS bf16* KTT = KE + 2560; LAS bf16* VT = KTT + 2304;
;     if (w < 4) {
;         const int k = lane & 31, half = lane >> 5;
;         float run = 0.f;
; #pragma unroll
;         for (int i = 0; i < 32; ++i) { run += __uint_as_float(__float_as_uint(in.bc[i]) << 16); in.bc[i] = run; }
;         const float tot0 = __shfl(run, k), tot1 = __shfl(run, 32 + k);
;         const float bref = tot0, blast = tot0 + tot1, off = half ? tot0 : 0.f;
;         const float sc = (w == 0 || w == 2) ? 0.17677669529663687f : 1.f;
; #pragma unroll
;         for (int i = 0; i < 32; ++i) { const int t = 32 * half + i; const float bi = in.bc[i] + off;
;             const float x = bf2f(in.px[i]) * sc;
;             const float ex = w == 0 ? bi - bref : (w == 1 ? bref - bi : (w == 2 ? bi : blast - bi));
;             const bf16 y = (bf16)f2bf(x * __expf(ex));
;             if (w == 0) QE[t * 40 + k] = y; else if (w == 1) KE[t * 40 + k] = y; else if (w == 2) QC[t * 32 + k] = y; else KTT[k * 72 + t] = y; }
;         if (w == 2 && half == 0) DL[k] = __expf(blast);
;     } else {
;         const int vv = 16 * (w - 4) + (lane & 15), tq = lane >> 4;
; #pragma unroll
;         for (int i = 0; i < 16; ++i) VT[vv * 72 + 16 * tq + i] = in.px[i];
;     }
;     asm volatile("s_waitcnt lgkmcnt(0)" ::: "memory");
; }
; __device__ __forceinline__ void gla_chain_units(CArgs& a, int chain, LAS unsigned char* lds, int w, int lane) {
;     ...
;         { gla_s1(a, chain * 36 + n + 1, B, lds + 24064, w, lane); __syncthreads(); if (n + 2 < 36) gla_fetch(a, chain * 36 + n + 2, w, lane, A); gla_s2(a, chain * 36 + n + 1, lds + 24064, w, lane); }
.LBB0_1024:
	s_add_i32 s78, s36, 0xffffee01
	s_andn2_b64 vcc, exec, s[2:3]
	s_lshl_b64 s[76:77], s[78:79], 12
	s_cbranch_vccnz .LBB0_1668
	v_add_f32_e32 v162, v62, v61
	v_add_f32_e32 v161, v157, v162
	v_add_f32_e32 v157, v155, v161
	v_add_f32_e32 v156, v156, v157
	v_add_f32_e32 v155, v153, v156
	v_add_f32_e32 v154, v154, v155
	v_add_f32_e32 v153, v151, v154
	v_add_f32_e32 v151, v152, v153
	v_add_f32_e32 v149, v149, v151
	v_add_f32_e32 v62, v150, v149
	v_add_f32_e32 v34, v82, v62
	v_add_f32_e32 v33, v83, v34
	v_add_f32_e32 v32, v80, v33
	v_add_f32_e32 v31, v81, v32
	v_add_f32_e32 v30, v78, v31
	v_add_f32_e32 v29, v79, v30
	v_add_f32_e32 v28, v76, v29
	v_add_f32_e32 v27, v77, v28
	v_add_f32_e32 v26, v74, v27
	v_add_f32_e32 v25, v75, v26
	v_add_f32_e32 v21, v72, v25
	v_add_f32_e32 v20, v73, v21
	v_add_f32_e32 v19, v70, v20
	v_add_f32_e32 v17, v71, v19
	v_add_f32_e32 v15, v68, v17
	v_add_f32_e32 v14, v69, v15
	v_add_f32_e32 v13, v66, v14
	v_add_f32_e32 v12, v67, v13
	v_add_f32_e32 v11, v64, v12
	v_and_b32_e32 v3, 31, v1
	v_add_f32_e32 v10, v65, v11
	v_and_or_b32 v2, v195, 64, v3
	v_add_f32_e32 v7, v63, v10
	v_lshlrev_b32_e32 v2, 2, v2
	ds_bpermute_b32 v5, v2, v7
	ds_bpermute_b32 v2, v2, v7 offset:128
	v_cmp_gt_u32_e64 s[48:49], 32, v1
	s_mov_b64 s[2:3], -1
	s_and_b64 vcc, exec, s[86:87]
	s_waitcnt lgkmcnt(1)
	v_cndmask_b32_e64 v8, v5, 0, s[48:49]
	s_waitcnt lgkmcnt(0)
	v_add_f32_e32 v4, v5, v2
	s_waitcnt vmcnt(9)
	v_lshl_add_u32 v232, v3, 1, 0
	s_movk_i32 s2, 0x8e
	v_mad_u32_u24 v233, v3, s2, v232
	v_and_b32_e32 v234, 0xffffffe0, v1
	v_readlane_b32 s3, v249, 3
	v_mov_b32_e32 v222, 1.0
	v_mov_b32_e32 v223, 0
	v_mad_u32_u24 v224, v234, s33, v232
	v_mov_b32_e32 v225, s33
	s_cmp_lg_u32 s3, 0
	s_cbranch_scc1 .LgsB_1
	v_xor_b32_e32 v223, 0x80000000, v5
.LgsB_1:
	s_cmp_lg_u32 s3, 1
	s_cbranch_scc1 .LgsB_2
	v_mov_b32_e32 v222, -1.0
	v_mov_b32_e32 v223, v5
	v_add_u32_e32 v224, 0x1400, v224
.LgsB_2:
	s_cmp_lg_u32 s3, 3
	s_cbranch_scc1 .LgsB_3
	v_mov_b32_e32 v222, -1.0
	v_mov_b32_e32 v223, v4
	v_lshl_add_u32 v224, v234, 1, v233
	v_add_u32_e32 v224, 0x2800, v224
	v_mov_b32_e32 v225, 2
.LgsB_3:
	v_add_u32_e32 v224, 0x5e00, v224
	s_cmp_eq_u32 s3, 2
	s_cbranch_scc1 .LgsB_qc
	v_add_f32_e32 v226, v61, v8
	v_add_f32_e32 v228, v162, v8
	v_fma_f32 v226, v226, v222, v223
	v_fma_f32 v228, v228, v222, v223
	v_mul_f32_e32 v226, 0x3fb8aa3b, v226
	v_mul_f32_e32 v228, 0x3fb8aa3b, v228
	v_exp_f32_e32 v226, v226
	v_exp_f32_e32 v228, v228
	v_lshlrev_b32_e32 v227, 16, v159
	v_lshlrev_b32_e32 v229, 16, v158
	v_mul_f32_e32 v227, v124, v227
	v_mul_f32_e32 v229, v124, v229
	v_mul_f32_e32 v226, v227, v226
	v_mul_f32_e32 v228, v229, v228
	v_cvt_pk_bf16_f32 v226, v226, v226
	v_cvt_pk_bf16_f32 v228, v228, v228
	ds_write_b16 v224, v226
	v_add_u32_e32 v224, v225, v224
	ds_write_b16 v224, v228
	v_add_u32_e32 v224, v225, v224
	v_add_f32_e32 v226, v161, v8
	v_add_f32_e32 v228, v157, v8
	v_fma_f32 v226, v226, v222, v223
	v_fma_f32 v228, v228, v222, v223
	v_mul_f32_e32 v226, 0x3fb8aa3b, v226
	v_mul_f32_e32 v228, 0x3fb8aa3b, v228
	v_exp_f32_e32 v226, v226
	v_exp_f32_e32 v228, v228
	v_lshlrev_b32_e32 v227, 16, v60
	v_lshlrev_b32_e32 v229, 16, v59
	v_mul_f32_e32 v227, v124, v227
	v_mul_f32_e32 v229, v124, v229
	v_mul_f32_e32 v226, v227, v226
	v_mul_f32_e32 v228, v229, v228
	v_cvt_pk_bf16_f32 v226, v226, v226
	v_cvt_pk_bf16_f32 v228, v228, v228
	ds_write_b16 v224, v226
	v_add_u32_e32 v224, v225, v224
	ds_write_b16 v224, v228
	v_add_u32_e32 v224, v225, v224
	v_add_f32_e32 v226, v156, v8
	v_add_f32_e32 v228, v155, v8
	v_fma_f32 v226, v226, v222, v223
	v_fma_f32 v228, v228, v222, v223
	v_mul_f32_e32 v226, 0x3fb8aa3b, v226
	v_mul_f32_e32 v228, 0x3fb8aa3b, v228
	v_exp_f32_e32 v226, v226
	v_exp_f32_e32 v228, v228
	v_lshlrev_b32_e32 v227, 16, v58
	v_lshlrev_b32_e32 v229, 16, v57
	v_mul_f32_e32 v227, v124, v227
	v_mul_f32_e32 v229, v124, v229
	v_mul_f32_e32 v226, v227, v226
	v_mul_f32_e32 v228, v229, v228
	v_cvt_pk_bf16_f32 v226, v226, v226
	v_cvt_pk_bf16_f32 v228, v228, v228
	ds_write_b16 v224, v226
	v_add_u32_e32 v224, v225, v224
	ds_write_b16 v224, v228
	v_add_u32_e32 v224, v225, v224
	v_add_f32_e32 v226, v154, v8
	v_add_f32_e32 v228, v153, v8
	v_fma_f32 v226, v226, v222, v223
	v_fma_f32 v228, v228, v222, v223
	v_mul_f32_e32 v226, 0x3fb8aa3b, v226
	v_mul_f32_e32 v228, 0x3fb8aa3b, v228
	v_exp_f32_e32 v226, v226
	v_exp_f32_e32 v228, v228
	v_lshlrev_b32_e32 v227, 16, v56
	v_lshlrev_b32_e32 v229, 16, v55
	v_mul_f32_e32 v227, v124, v227
	v_mul_f32_e32 v229, v124, v229
	v_mul_f32_e32 v226, v227, v226
	v_mul_f32_e32 v228, v229, v228
	v_cvt_pk_bf16_f32 v226, v226, v226
	v_cvt_pk_bf16_f32 v228, v228, v228
	ds_write_b16 v224, v226
	v_add_u32_e32 v224, v225, v224
	ds_write_b16 v224, v228
	v_add_u32_e32 v224, v225, v224
	v_add_f32_e32 v226, v151, v8
	v_add_f32_e32 v228, v149, v8
	v_fma_f32 v226, v226, v222, v223
	v_fma_f32 v228, v228, v222, v223
	v_mul_f32_e32 v226, 0x3fb8aa3b, v226
	v_mul_f32_e32 v228, 0x3fb8aa3b, v228
	v_exp_f32_e32 v226, v226
	v_exp_f32_e32 v228, v228
	v_lshlrev_b32_e32 v227, 16, v54
	v_lshlrev_b32_e32 v229, 16, v53
	v_mul_f32_e32 v227, v124, v227
	v_mul_f32_e32 v229, v124, v229
	v_mul_f32_e32 v226, v227, v226
	v_mul_f32_e32 v228, v229, v228
	v_cvt_pk_bf16_f32 v226, v226, v226
	v_cvt_pk_bf16_f32 v228, v228, v228
	ds_write_b16 v224, v226
	v_add_u32_e32 v224, v225, v224
	ds_write_b16 v224, v228
	v_add_u32_e32 v224, v225, v224
	v_add_f32_e32 v226, v62, v8
	v_add_f32_e32 v228, v34, v8
	v_fma_f32 v226, v226, v222, v223
	v_fma_f32 v228, v228, v222, v223
	v_mul_f32_e32 v226, 0x3fb8aa3b, v226
	v_mul_f32_e32 v228, 0x3fb8aa3b, v228
	v_exp_f32_e32 v226, v226
	v_exp_f32_e32 v228, v228
; __device__ __forceinline__ float bf2f(unsigned v) { return __uint_as_float(v << 16); }
; __device__ __forceinline__ unsigned f2bf(float f) { unsigned u = __float_as_uint(f); return (u + 0x7fffu + ((u >> 16) & 1u)) >> 16; }
; __device__ __forceinline__ void gla_s1(CArgs& a, int u, GlaIn& in, LAS unsigned char* ub, int w, int lane) {
;     ...
;         for (int i = 0; i < 32; ++i) { const int t = 32 * half + i; const float bi = in.bc[i] + off;
;             const float x = bf2f(in.px[i]) * sc;
;             const float ex = w == 0 ? bi - bref : (w == 1 ? bref - bi : (w == 2 ? bi : blast - bi));
;             const bf16 y = (bf16)f2bf(x * __expf(ex));
;             if (w == 0) QE[t * 40 + k] = y; else if (w == 1) KE[t * 40 + k] = y; else if (w == 2) QC[t * 32 + k] = y; else KTT[k * 72 + t] = y; }
	v_lshlrev_b32_e32 v227, 16, v43
	v_lshlrev_b32_e32 v229, 16, v24
	v_mul_f32_e32 v227, v124, v227
	v_mul_f32_e32 v229, v124, v229
	v_mul_f32_e32 v226, v227, v226
	v_mul_f32_e32 v228, v229, v228
	v_cvt_pk_bf16_f32 v226, v226, v226
	v_cvt_pk_bf16_f32 v228, v228, v228
	ds_write_b16 v224, v226
	v_add_u32_e32 v224, v225, v224
	ds_write_b16 v224, v228
	v_add_u32_e32 v224, v225, v224
	v_add_f32_e32 v226, v33, v8
	v_add_f32_e32 v228, v32, v8
	v_fma_f32 v226, v226, v222, v223
	v_fma_f32 v228, v228, v222, v223
	v_mul_f32_e32 v226, 0x3fb8aa3b, v226
	v_mul_f32_e32 v228, 0x3fb8aa3b, v228
	v_exp_f32_e32 v226, v226
	v_exp_f32_e32 v228, v228
	v_lshlrev_b32_e32 v227, 16, v23
	v_lshlrev_b32_e32 v229, 16, v22
	v_mul_f32_e32 v227, v124, v227
	v_mul_f32_e32 v229, v124, v229
	v_mul_f32_e32 v226, v227, v226
	v_mul_f32_e32 v228, v229, v228
	v_cvt_pk_bf16_f32 v226, v226, v226
	v_cvt_pk_bf16_f32 v228, v228, v228
	ds_write_b16 v224, v226
	v_add_u32_e32 v224, v225, v224
	ds_write_b16 v224, v228
	v_add_u32_e32 v224, v225, v224
	v_add_f32_e32 v226, v31, v8
	v_add_f32_e32 v228, v30, v8
	v_fma_f32 v226, v226, v222, v223
	v_fma_f32 v228, v228, v222, v223
	v_mul_f32_e32 v226, 0x3fb8aa3b, v226
	v_mul_f32_e32 v228, 0x3fb8aa3b, v228
	v_exp_f32_e32 v226, v226
	v_exp_f32_e32 v228, v228
	v_lshlrev_b32_e32 v227, 16, v18
	v_lshlrev_b32_e32 v229, 16, v16
	v_mul_f32_e32 v227, v124, v227
	v_mul_f32_e32 v229, v124, v229
	v_mul_f32_e32 v226, v227, v226
	v_mul_f32_e32 v228, v229, v228
	v_cvt_pk_bf16_f32 v226, v226, v226
	v_cvt_pk_bf16_f32 v228, v228, v228
	ds_write_b16 v224, v226
	v_add_u32_e32 v224, v225, v224
	ds_write_b16 v224, v228
	v_add_u32_e32 v224, v225, v224
	v_add_f32_e32 v226, v29, v8
	v_add_f32_e32 v228, v28, v8
	v_fma_f32 v226, v226, v222, v223
	v_fma_f32 v228, v228, v222, v223
	v_mul_f32_e32 v226, 0x3fb8aa3b, v226
	v_mul_f32_e32 v228, 0x3fb8aa3b, v228
	v_exp_f32_e32 v226, v226
	v_exp_f32_e32 v228, v228
	v_mov_b32_e32 v227, v52
	v_mov_b32_e32 v229, v51
	v_mul_f32_e32 v227, v124, v227
	v_mul_f32_e32 v229, v124, v229
	v_mul_f32_e32 v226, v227, v226
	v_mul_f32_e32 v228, v229, v228
	v_cvt_pk_bf16_f32 v226, v226, v226
	v_cvt_pk_bf16_f32 v228, v228, v228
	ds_write_b16 v224, v226
	v_add_u32_e32 v224, v225, v224
	ds_write_b16 v224, v228
	v_add_u32_e32 v224, v225, v224
	v_add_f32_e32 v226, v27, v8
	v_add_f32_e32 v228, v26, v8
	v_fma_f32 v226, v226, v222, v223
	v_fma_f32 v228, v228, v222, v223
	v_mul_f32_e32 v226, 0x3fb8aa3b, v226
	v_mul_f32_e32 v228, 0x3fb8aa3b, v228
	v_exp_f32_e32 v226, v226
	v_exp_f32_e32 v228, v228
	v_mov_b32_e32 v227, v50
	v_mov_b32_e32 v229, v49
	v_mul_f32_e32 v227, v124, v227
	v_mul_f32_e32 v229, v124, v229
	v_mul_f32_e32 v226, v227, v226
	v_mul_f32_e32 v228, v229, v228
	v_cvt_pk_bf16_f32 v226, v226, v226
	v_cvt_pk_bf16_f32 v228, v228, v228
	ds_write_b16 v224, v226
	v_add_u32_e32 v224, v225, v224
	ds_write_b16 v224, v228
	v_add_u32_e32 v224, v225, v224
	v_add_f32_e32 v226, v25, v8
	v_add_f32_e32 v228, v21, v8
	v_fma_f32 v226, v226, v222, v223
	v_fma_f32 v228, v228, v222, v223
	v_mul_f32_e32 v226, 0x3fb8aa3b, v226
	v_mul_f32_e32 v228, 0x3fb8aa3b, v228
	v_exp_f32_e32 v226, v226
	v_exp_f32_e32 v228, v228
	v_mov_b32_e32 v227, v48
	v_mov_b32_e32 v229, v47
	v_mul_f32_e32 v227, v124, v227
	v_mul_f32_e32 v229, v124, v229
	v_mul_f32_e32 v226, v227, v226
	v_mul_f32_e32 v228, v229, v228
	v_cvt_pk_bf16_f32 v226, v226, v226
	v_cvt_pk_bf16_f32 v228, v228, v228
	ds_write_b16 v224, v226
	v_add_u32_e32 v224, v225, v224
	ds_write_b16 v224, v228
	v_add_u32_e32 v224, v225, v224
	v_add_f32_e32 v226, v20, v8
	v_add_f32_e32 v228, v19, v8
	v_fma_f32 v226, v226, v222, v223
	v_fma_f32 v228, v228, v222, v223
	v_mul_f32_e32 v226, 0x3fb8aa3b, v226
	v_mul_f32_e32 v228, 0x3fb8aa3b, v228
	v_exp_f32_e32 v226, v226
	v_exp_f32_e32 v228, v228
	v_mov_b32_e32 v227, v46
	v_mov_b32_e32 v229, v45
	v_mul_f32_e32 v227, v124, v227
	v_mul_f32_e32 v229, v124, v229
	v_mul_f32_e32 v226, v227, v226
	v_mul_f32_e32 v228, v229, v228
	v_cvt_pk_bf16_f32 v226, v226, v226
	v_cvt_pk_bf16_f32 v228, v228, v228
	ds_write_b16 v224, v226
	v_add_u32_e32 v224, v225, v224
	ds_write_b16 v224, v228
	v_add_u32_e32 v224, v225, v224
	v_add_f32_e32 v226, v17, v8
	v_add_f32_e32 v228, v15, v8
	v_fma_f32 v226, v226, v222, v223
	v_fma_f32 v228, v228, v222, v223
	v_mul_f32_e32 v226, 0x3fb8aa3b, v226
	v_mul_f32_e32 v228, 0x3fb8aa3b, v228
	v_exp_f32_e32 v226, v226
	v_exp_f32_e32 v228, v228
	v_mov_b32_e32 v227, v44
	v_mov_b32_e32 v229, v42
	v_mul_f32_e32 v227, v124, v227
	v_mul_f32_e32 v229, v124, v229
	v_mul_f32_e32 v226, v227, v226
	v_mul_f32_e32 v228, v229, v228
	v_cvt_pk_bf16_f32 v226, v226, v226
	v_cvt_pk_bf16_f32 v228, v228, v228
	ds_write_b16 v224, v226
	v_add_u32_e32 v224, v225, v224
	ds_write_b16 v224, v228
	v_add_u32_e32 v224, v225, v224
	v_add_f32_e32 v226, v14, v8
	v_add_f32_e32 v228, v13, v8
	v_fma_f32 v226, v226, v222, v223
	v_fma_f32 v228, v228, v222, v223
	v_mul_f32_e32 v226, 0x3fb8aa3b, v226
	v_mul_f32_e32 v228, 0x3fb8aa3b, v228
	v_exp_f32_e32 v226, v226
	v_exp_f32_e32 v228, v228
	v_mov_b32_e32 v227, v41
	v_mov_b32_e32 v229, v40
	v_mul_f32_e32 v227, v124, v227
	v_mul_f32_e32 v229, v124, v229
	v_mul_f32_e32 v226, v227, v226
	v_mul_f32_e32 v228, v229, v228
	v_cvt_pk_bf16_f32 v226, v226, v226
	v_cvt_pk_bf16_f32 v228, v228, v228
	ds_write_b16 v224, v226
	v_add_u32_e32 v224, v225, v224
	ds_write_b16 v224, v228
	v_add_u32_e32 v224, v225, v224
	v_add_f32_e32 v226, v12, v8
	v_add_f32_e32 v228, v11, v8
	v_fma_f32 v226, v226, v222, v223
	v_fma_f32 v228, v228, v222, v223
	v_mul_f32_e32 v226, 0x3fb8aa3b, v226
	v_mul_f32_e32 v228, 0x3fb8aa3b, v228
	v_exp_f32_e32 v226, v226
	v_exp_f32_e32 v228, v228
	v_mov_b32_e32 v227, v39
	v_mov_b32_e32 v229, v38
	v_mul_f32_e32 v227, v124, v227
	v_mul_f32_e32 v229, v124, v229
	v_mul_f32_e32 v226, v227, v226
	v_mul_f32_e32 v228, v229, v228
	v_cvt_pk_bf16_f32 v226, v226, v226
	v_cvt_pk_bf16_f32 v228, v228, v228
	ds_write_b16 v224, v226
	v_add_u32_e32 v224, v225, v224
	ds_write_b16 v224, v228
	v_add_u32_e32 v224, v225, v224
	v_add_f32_e32 v226, v10, v8
	v_add_f32_e32 v228, v7, v8
	v_fma_f32 v226, v226, v222, v223
	v_fma_f32 v228, v228, v222, v223
	v_mul_f32_e32 v226, 0x3fb8aa3b, v226
	v_mul_f32_e32 v228, 0x3fb8aa3b, v228
	v_exp_f32_e32 v226, v226
	v_exp_f32_e32 v228, v228
	v_mov_b32_e32 v227, v37
	v_mov_b32_e32 v229, v36
	v_mul_f32_e32 v227, v124, v227
	v_mul_f32_e32 v229, v124, v229
	v_mul_f32_e32 v226, v227, v226
	v_mul_f32_e32 v228, v229, v228
	v_cvt_pk_bf16_f32 v226, v226, v226
	v_cvt_pk_bf16_f32 v228, v228, v228
	ds_write_b16 v224, v226
	v_add_u32_e32 v224, v225, v224
	ds_write_b16 v224, v228
	v_add_u32_e32 v224, v225, v224
	s_branch .LgsB_end
; __device__ __forceinline__ float bf2f(unsigned v) { return __uint_as_float(v << 16); }
; __device__ __forceinline__ unsigned f2bf(float f) { unsigned u = __float_as_uint(f); return (u + 0x7fffu + ((u >> 16) & 1u)) >> 16; }
; __device__ __forceinline__ void gla_s1(CArgs& a, int u, GlaIn& in, LAS unsigned char* ub, int w, int lane) {
;     ...
;         for (int i = 0; i < 32; ++i) { const int t = 32 * half + i; const float bi = in.bc[i] + off;
;             const float x = bf2f(in.px[i]) * sc;
;             const float ex = w == 0 ? bi - bref : (w == 1 ? bref - bi : (w == 2 ? bi : blast - bi));
;             const bf16 y = (bf16)f2bf(x * __expf(ex));
;             if (w == 0) QE[t * 40 + k] = y; else if (w == 1) KE[t * 40 + k] = y; else if (w == 2) QC[t * 32 + k] = y; else KTT[k * 72 + t] = y; }
;         if (w == 2 && half == 0) DL[k] = __expf(blast);
.LgsB_qc:
	v_readlane_b32 s2, v249, 22
	v_readlane_b32 s3, v249, 23
	s_add_u32 s2, s2, s76
	s_addc_u32 s3, s3, s77
	v_lshl_or_b32 v230, v234, 5, v3
	v_mov_b32_e32 v231, 0
	v_lshl_add_u64 v[230:231], v[230:231], 1, s[2:3]
	v_add_f32_e32 v226, v61, v8
	v_add_f32_e32 v228, v162, v8
	v_fma_f32 v226, v226, v222, v223
	v_fma_f32 v228, v228, v222, v223
	v_mul_f32_e32 v226, 0x3fb8aa3b, v226
	v_mul_f32_e32 v228, 0x3fb8aa3b, v228
	v_exp_f32_e32 v226, v226
	v_exp_f32_e32 v228, v228
	v_lshlrev_b32_e32 v227, 16, v159
	v_lshlrev_b32_e32 v229, 16, v158
	v_mul_f32_e32 v227, v124, v227
	v_mul_f32_e32 v229, v124, v229
	v_mul_f32_e32 v226, v227, v226
	v_mul_f32_e32 v228, v229, v228
	v_cvt_pk_bf16_f32 v226, v226, v226
	v_cvt_pk_bf16_f32 v228, v228, v228
	global_store_short v[230:231], v226, off
	global_store_short v[230:231], v228, off offset:64
	v_add_f32_e32 v226, v161, v8
	v_add_f32_e32 v228, v157, v8
	v_fma_f32 v226, v226, v222, v223
	v_fma_f32 v228, v228, v222, v223
	v_mul_f32_e32 v226, 0x3fb8aa3b, v226
	v_mul_f32_e32 v228, 0x3fb8aa3b, v228
	v_exp_f32_e32 v226, v226
	v_exp_f32_e32 v228, v228
	v_lshlrev_b32_e32 v227, 16, v60
	v_lshlrev_b32_e32 v229, 16, v59
	v_mul_f32_e32 v227, v124, v227
	v_mul_f32_e32 v229, v124, v229
	v_mul_f32_e32 v226, v227, v226
	v_mul_f32_e32 v228, v229, v228
	v_cvt_pk_bf16_f32 v226, v226, v226
	v_cvt_pk_bf16_f32 v228, v228, v228
	global_store_short v[230:231], v226, off offset:128
	global_store_short v[230:231], v228, off offset:192
	v_add_f32_e32 v226, v156, v8
	v_add_f32_e32 v228, v155, v8
	v_fma_f32 v226, v226, v222, v223
	v_fma_f32 v228, v228, v222, v223
	v_mul_f32_e32 v226, 0x3fb8aa3b, v226
	v_mul_f32_e32 v228, 0x3fb8aa3b, v228
	v_exp_f32_e32 v226, v226
	v_exp_f32_e32 v228, v228
	v_lshlrev_b32_e32 v227, 16, v58
	v_lshlrev_b32_e32 v229, 16, v57
	v_mul_f32_e32 v227, v124, v227
	v_mul_f32_e32 v229, v124, v229
	v_mul_f32_e32 v226, v227, v226
	v_mul_f32_e32 v228, v229, v228
	v_cvt_pk_bf16_f32 v226, v226, v226
	v_cvt_pk_bf16_f32 v228, v228, v228
	global_store_short v[230:231], v226, off offset:256
	global_store_short v[230:231], v228, off offset:320
	v_add_f32_e32 v226, v154, v8
	v_add_f32_e32 v228, v153, v8
	v_fma_f32 v226, v226, v222, v223
	v_fma_f32 v228, v228, v222, v223
	v_mul_f32_e32 v226, 0x3fb8aa3b, v226
	v_mul_f32_e32 v228, 0x3fb8aa3b, v228
	v_exp_f32_e32 v226, v226
	v_exp_f32_e32 v228, v228
	v_lshlrev_b32_e32 v227, 16, v56
	v_lshlrev_b32_e32 v229, 16, v55
	v_mul_f32_e32 v227, v124, v227
	v_mul_f32_e32 v229, v124, v229
	v_mul_f32_e32 v226, v227, v226
	v_mul_f32_e32 v228, v229, v228
	v_cvt_pk_bf16_f32 v226, v226, v226
	v_cvt_pk_bf16_f32 v228, v228, v228
	global_store_short v[230:231], v226, off offset:384
	global_store_short v[230:231], v228, off offset:448
	v_add_f32_e32 v226, v151, v8
	v_add_f32_e32 v228, v149, v8
	v_fma_f32 v226, v226, v222, v223
	v_fma_f32 v228, v228, v222, v223
	v_mul_f32_e32 v226, 0x3fb8aa3b, v226
	v_mul_f32_e32 v228, 0x3fb8aa3b, v228
	v_exp_f32_e32 v226, v226
	v_exp_f32_e32 v228, v228
	v_lshlrev_b32_e32 v227, 16, v54
	v_lshlrev_b32_e32 v229, 16, v53
	v_mul_f32_e32 v227, v124, v227
	v_mul_f32_e32 v229, v124, v229
	v_mul_f32_e32 v226, v227, v226
	v_mul_f32_e32 v228, v229, v228
	v_cvt_pk_bf16_f32 v226, v226, v226
	v_cvt_pk_bf16_f32 v228, v228, v228
	global_store_short v[230:231], v226, off offset:512
	global_store_short v[230:231], v228, off offset:576
	v_add_f32_e32 v226, v62, v8
	v_add_f32_e32 v228, v34, v8
	v_fma_f32 v226, v226, v222, v223
	v_fma_f32 v228, v228, v222, v223
	v_mul_f32_e32 v226, 0x3fb8aa3b, v226
	v_mul_f32_e32 v228, 0x3fb8aa3b, v228
	v_exp_f32_e32 v226, v226
	v_exp_f32_e32 v228, v228
	v_lshlrev_b32_e32 v227, 16, v43
	v_lshlrev_b32_e32 v229, 16, v24
	v_mul_f32_e32 v227, v124, v227
	v_mul_f32_e32 v229, v124, v229
	v_mul_f32_e32 v226, v227, v226
	v_mul_f32_e32 v228, v229, v228
	v_cvt_pk_bf16_f32 v226, v226, v226
	v_cvt_pk_bf16_f32 v228, v228, v228
	global_store_short v[230:231], v226, off offset:640
	global_store_short v[230:231], v228, off offset:704
	v_add_f32_e32 v226, v33, v8
	v_add_f32_e32 v228, v32, v8
	v_fma_f32 v226, v226, v222, v223
	v_fma_f32 v228, v228, v222, v223
	v_mul_f32_e32 v226, 0x3fb8aa3b, v226
	v_mul_f32_e32 v228, 0x3fb8aa3b, v228
	v_exp_f32_e32 v226, v226
	v_exp_f32_e32 v228, v228
	v_lshlrev_b32_e32 v227, 16, v23
	v_lshlrev_b32_e32 v229, 16, v22
	v_mul_f32_e32 v227, v124, v227
	v_mul_f32_e32 v229, v124, v229
	v_mul_f32_e32 v226, v227, v226
	v_mul_f32_e32 v228, v229, v228
	v_cvt_pk_bf16_f32 v226, v226, v226
	v_cvt_pk_bf16_f32 v228, v228, v228
	global_store_short v[230:231], v226, off offset:768
	global_store_short v[230:231], v228, off offset:832
	v_add_f32_e32 v226, v31, v8
	v_add_f32_e32 v228, v30, v8
	v_fma_f32 v226, v226, v222, v223
	v_fma_f32 v228, v228, v222, v223
	v_mul_f32_e32 v226, 0x3fb8aa3b, v226
	v_mul_f32_e32 v228, 0x3fb8aa3b, v228
	v_exp_f32_e32 v226, v226
	v_exp_f32_e32 v228, v228
	v_lshlrev_b32_e32 v227, 16, v18
	v_lshlrev_b32_e32 v229, 16, v16
	v_mul_f32_e32 v227, v124, v227
	v_mul_f32_e32 v229, v124, v229
	v_mul_f32_e32 v226, v227, v226
	v_mul_f32_e32 v228, v229, v228
	v_cvt_pk_bf16_f32 v226, v226, v226
	v_cvt_pk_bf16_f32 v228, v228, v228
; __device__ __forceinline__ float bf2f(unsigned v) { return __uint_as_float(v << 16); }
; __device__ __forceinline__ unsigned f2bf(float f) { unsigned u = __float_as_uint(f); return (u + 0x7fffu + ((u >> 16) & 1u)) >> 16; }
; __device__ __forceinline__ void gla_s1(CArgs& a, int u, GlaIn& in, LAS unsigned char* ub, int w, int lane) {
;     ...
;         for (int i = 0; i < 32; ++i) { const int t = 32 * half + i; const float bi = in.bc[i] + off;
;             const float x = bf2f(in.px[i]) * sc;
;             const float ex = w == 0 ? bi - bref : (w == 1 ? bref - bi : (w == 2 ? bi : blast - bi));
;             const bf16 y = (bf16)f2bf(x * __expf(ex));
;             if (w == 0) QE[t * 40 + k] = y; else if (w == 1) KE[t * 40 + k] = y; else if (w == 2) QC[t * 32 + k] = y; else KTT[k * 72 + t] = y; }
;         if (w == 2 && half == 0) DL[k] = __expf(blast);
	global_store_short v[230:231], v226, off offset:896
	global_store_short v[230:231], v228, off offset:960
	v_add_f32_e32 v226, v29, v8
	v_add_f32_e32 v228, v28, v8
	v_fma_f32 v226, v226, v222, v223
	v_fma_f32 v228, v228, v222, v223
	v_mul_f32_e32 v226, 0x3fb8aa3b, v226
	v_mul_f32_e32 v228, 0x3fb8aa3b, v228
	v_exp_f32_e32 v226, v226
	v_exp_f32_e32 v228, v228
	v_mov_b32_e32 v227, v52
	v_mov_b32_e32 v229, v51
	v_mul_f32_e32 v227, v124, v227
	v_mul_f32_e32 v229, v124, v229
	v_mul_f32_e32 v226, v227, v226
	v_mul_f32_e32 v228, v229, v228
	v_cvt_pk_bf16_f32 v226, v226, v226
	v_cvt_pk_bf16_f32 v228, v228, v228
	global_store_short v[230:231], v226, off offset:1024
	global_store_short v[230:231], v228, off offset:1088
	v_add_f32_e32 v226, v27, v8
	v_add_f32_e32 v228, v26, v8
	v_fma_f32 v226, v226, v222, v223
	v_fma_f32 v228, v228, v222, v223
	v_mul_f32_e32 v226, 0x3fb8aa3b, v226
	v_mul_f32_e32 v228, 0x3fb8aa3b, v228
	v_exp_f32_e32 v226, v226
	v_exp_f32_e32 v228, v228
	v_mov_b32_e32 v227, v50
	v_mov_b32_e32 v229, v49
	v_mul_f32_e32 v227, v124, v227
	v_mul_f32_e32 v229, v124, v229
	v_mul_f32_e32 v226, v227, v226
	v_mul_f32_e32 v228, v229, v228
	v_cvt_pk_bf16_f32 v226, v226, v226
	v_cvt_pk_bf16_f32 v228, v228, v228
	global_store_short v[230:231], v226, off offset:1152
	global_store_short v[230:231], v228, off offset:1216
	v_add_f32_e32 v226, v25, v8
	v_add_f32_e32 v228, v21, v8
	v_fma_f32 v226, v226, v222, v223
	v_fma_f32 v228, v228, v222, v223
	v_mul_f32_e32 v226, 0x3fb8aa3b, v226
	v_mul_f32_e32 v228, 0x3fb8aa3b, v228
	v_exp_f32_e32 v226, v226
	v_exp_f32_e32 v228, v228
	v_mov_b32_e32 v227, v48
	v_mov_b32_e32 v229, v47
	v_mul_f32_e32 v227, v124, v227
	v_mul_f32_e32 v229, v124, v229
	v_mul_f32_e32 v226, v227, v226
	v_mul_f32_e32 v228, v229, v228
	v_cvt_pk_bf16_f32 v226, v226, v226
	v_cvt_pk_bf16_f32 v228, v228, v228
	global_store_short v[230:231], v226, off offset:1280
	global_store_short v[230:231], v228, off offset:1344
	v_add_f32_e32 v226, v20, v8
	v_add_f32_e32 v228, v19, v8
	v_fma_f32 v226, v226, v222, v223
	v_fma_f32 v228, v228, v222, v223
	v_mul_f32_e32 v226, 0x3fb8aa3b, v226
	v_mul_f32_e32 v228, 0x3fb8aa3b, v228
	v_exp_f32_e32 v226, v226
	v_exp_f32_e32 v228, v228
	v_mov_b32_e32 v227, v46
	v_mov_b32_e32 v229, v45
	v_mul_f32_e32 v227, v124, v227
	v_mul_f32_e32 v229, v124, v229
	v_mul_f32_e32 v226, v227, v226
	v_mul_f32_e32 v228, v229, v228
	v_cvt_pk_bf16_f32 v226, v226, v226
	v_cvt_pk_bf16_f32 v228, v228, v228
	global_store_short v[230:231], v226, off offset:1408
	global_store_short v[230:231], v228, off offset:1472
	v_add_f32_e32 v226, v17, v8
	v_add_f32_e32 v228, v15, v8
	v_fma_f32 v226, v226, v222, v223
	v_fma_f32 v228, v228, v222, v223
	v_mul_f32_e32 v226, 0x3fb8aa3b, v226
	v_mul_f32_e32 v228, 0x3fb8aa3b, v228
	v_exp_f32_e32 v226, v226
	v_exp_f32_e32 v228, v228
	v_mov_b32_e32 v227, v44
	v_mov_b32_e32 v229, v42
	v_mul_f32_e32 v227, v124, v227
	v_mul_f32_e32 v229, v124, v229
	v_mul_f32_e32 v226, v227, v226
	v_mul_f32_e32 v228, v229, v228
	v_cvt_pk_bf16_f32 v226, v226, v226
	v_cvt_pk_bf16_f32 v228, v228, v228
	global_store_short v[230:231], v226, off offset:1536
	global_store_short v[230:231], v228, off offset:1600
	v_add_f32_e32 v226, v14, v8
	v_add_f32_e32 v228, v13, v8
	v_fma_f32 v226, v226, v222, v223
	v_fma_f32 v228, v228, v222, v223
	v_mul_f32_e32 v226, 0x3fb8aa3b, v226
	v_mul_f32_e32 v228, 0x3fb8aa3b, v228
	v_exp_f32_e32 v226, v226
	v_exp_f32_e32 v228, v228
	v_mov_b32_e32 v227, v41
	v_mov_b32_e32 v229, v40
	v_mul_f32_e32 v227, v124, v227
	v_mul_f32_e32 v229, v124, v229
	v_mul_f32_e32 v226, v227, v226
	v_mul_f32_e32 v228, v229, v228
	v_cvt_pk_bf16_f32 v226, v226, v226
	v_cvt_pk_bf16_f32 v228, v228, v228
	global_store_short v[230:231], v226, off offset:1664
	global_store_short v[230:231], v228, off offset:1728
	v_add_f32_e32 v226, v12, v8
	v_add_f32_e32 v228, v11, v8
	v_fma_f32 v226, v226, v222, v223
	v_fma_f32 v228, v228, v222, v223
	v_mul_f32_e32 v226, 0x3fb8aa3b, v226
	v_mul_f32_e32 v228, 0x3fb8aa3b, v228
	v_exp_f32_e32 v226, v226
	v_exp_f32_e32 v228, v228
	v_mov_b32_e32 v227, v39
	v_mov_b32_e32 v229, v38
	v_mul_f32_e32 v227, v124, v227
	v_mul_f32_e32 v229, v124, v229
	v_mul_f32_e32 v226, v227, v226
	v_mul_f32_e32 v228, v229, v228
	v_cvt_pk_bf16_f32 v226, v226, v226
	v_cvt_pk_bf16_f32 v228, v228, v228
	global_store_short v[230:231], v226, off offset:1792
	global_store_short v[230:231], v228, off offset:1856
	v_add_f32_e32 v226, v10, v8
	v_add_f32_e32 v228, v7, v8
	v_fma_f32 v226, v226, v222, v223
	v_fma_f32 v228, v228, v222, v223
	v_mul_f32_e32 v226, 0x3fb8aa3b, v226
	v_mul_f32_e32 v228, 0x3fb8aa3b, v228
	v_exp_f32_e32 v226, v226
	v_exp_f32_e32 v228, v228
	v_mov_b32_e32 v227, v37
	v_mov_b32_e32 v229, v36
	v_mul_f32_e32 v227, v124, v227
	v_mul_f32_e32 v229, v124, v229
	v_mul_f32_e32 v226, v227, v226
	v_mul_f32_e32 v228, v229, v228
	v_cvt_pk_bf16_f32 v226, v226, v226
	v_cvt_pk_bf16_f32 v228, v228, v228
	global_store_short v[230:231], v226, off offset:1920
	global_store_short v[230:231], v228, off offset:1984
.LgsB_end:
.LBB0_1665:
	s_and_b64 s[48:49], s[40:41], s[48:49]
	s_and_saveexec_b64 s[2:3], s[48:49]
	s_cbranch_execz .LBB0_1667

; #define LAS __attribute__((address_space(3)))
; __device__ __forceinline__ void cvb_load(CArgs& a, int l, int bit, int w, int lane, CvbRegs& r) {
;     const int kbb = bit & 7, nb = (bit >> 3) & 3, m = bit >> 5, e = m / 3, which = m - 3 * e;
;     const float* W = a.in[which == 0 ? I_WG : (which == 1 ? I_WU : I_WD)] + ((size_t)(l * NEXP + e)) * 1024 * 1024 + (size_t)(128 * kbb + 16 * w) * 1024 + 256 * nb + 4 * lane;
; #pragma unroll
;     for (int j = 0; j < 16; ++j) r.t[j] = *(const f32x4*)(W + (size_t)j * 1024);
; __device__ __forceinline__ void ph_scan(CArgs& a, int l, LAS unsigned char* lds, int bid, int nblk, unsigned long long& tacc) {
;     ...
;     {
;         LAS unsigned char* scr = lds + w * 8448;
;         if (nblk == 256) { const int per = bid < 128 ? 8 : 16, first = bid < 128 ? bid * 8 : 1024 + (bid - 128) * 16;
;             CvbRegs r0, r1;
;             cvb_load(a, l, first, w, lane, r0);
; #pragma unroll 1
;             for (int it = first; it < first + per; it += 2) {
;                 cvb_load(a, l, it + 1, w, lane, r1);
;                 cvb_store(a, it, w, lane, r0, lds);
;                 cvb_load(a, l, min(it + 2, first + per - 1), w, lane, r0);
;                 cvb_store(a, it + 1, w, lane, r1, lds + 36864); } }
.LBB0_2662:
	s_andn2_b64 vcc, exec, s[2:3]
	s_cbranch_vccnz .LBB0_2697
	v_readlane_b32 s0, v251, 7
	s_cmpk_lt_i32 s0, 0x80
	s_cbranch_scc1 .LBB0_2697
	v_readlane_b32 s0, v252, 55
	s_load_dwordx2 s[2:3], s[30:31], s0 offset:0x0
	s_lshl_b32 s0, s84, 5
	v_readlane_b32 s1, v252, 26
	s_add_i32 s4, s0, s1
	s_ashr_i32 s5, s4, 31
	s_lshl_b64 s[4:5], s[4:5], 22
	s_waitcnt lgkmcnt(0)
	s_add_u32 s1, s2, s4
	v_readlane_b32 s2, v249, 3
	s_addc_u32 s6, s3, s5
	s_lshl_b32 s2, s2, 4
	s_ashr_i32 s3, s2, 31
	s_lshl_b64 s[4:5], s[2:3], 12
	s_add_u32 s1, s1, s4
	s_addc_u32 s3, s6, s5
	v_readlane_b32 s4, v252, 56
	s_add_u32 s4, s1, s4
	s_addc_u32 s5, s3, 0
	v_lshlrev_b32_e32 v34, 4, v160
	s_waitcnt vmcnt(0)
	v_lshl_add_u64 v[64:65], s[4:5], 0, v[34:35]
	s_movk_i32 s1, 0x2000
	s_waitcnt vmcnt(0)
	v_add_co_u32_e32 v6, vcc, s1, v64
	s_movk_i32 s1, 0x4000
	s_nop 0
	v_addc_co_u32_e32 v7, vcc, 0, v65, vcc
	global_load_dwordx4 v[2:5], v34, s[4:5]
	global_load_dwordx4 v[10:13], v[6:7], off offset:-4096
	global_load_dwordx4 v[14:17], v[6:7], off
	v_add_co_u32_e32 v6, vcc, s1, v64
	s_movk_i32 s1, 0x6000
	s_nop 0
	v_addc_co_u32_e32 v7, vcc, 0, v65, vcc
	global_load_dwordx4 v[30:33], v[6:7], off offset:-4096
	global_load_dwordx4 v[18:21], v[6:7], off
	v_add_co_u32_e32 v6, vcc, s1, v64
	s_mov_b32 s1, 0x8000
	s_nop 0
	v_addc_co_u32_e32 v7, vcc, 0, v65, vcc
	global_load_dwordx4 v[40:43], v[6:7], off offset:-4096
	global_load_dwordx4 v[44:47], v[6:7], off
	v_add_co_u32_e32 v6, vcc, s1, v64
	s_mov_b32 s1, 0xa000
	s_nop 0
	v_addc_co_u32_e32 v7, vcc, 0, v65, vcc
	v_add_co_u32_e32 v26, vcc, s1, v64
	s_mov_b32 s1, 0xc000
	s_nop 0
	v_addc_co_u32_e32 v27, vcc, 0, v65, vcc
	v_add_co_u32_e32 v36, vcc, s1, v64
	s_mov_b32 s1, 0xe000
	s_nop 0
	v_addc_co_u32_e32 v37, vcc, 0, v65, vcc
	v_add_co_u32_e32 v56, vcc, s1, v64
	s_mov_b32 s1, 0xf000
	s_nop 0
	v_addc_co_u32_e32 v57, vcc, 0, v65, vcc
	v_add_co_u32_e32 v64, vcc, s1, v64
	global_load_dwordx4 v[60:63], v[6:7], off offset:-4096
	s_nop 0
	global_load_dwordx4 v[6:9], v[6:7], off
	v_addc_co_u32_e32 v65, vcc, 0, v65, vcc
	global_load_dwordx4 v[22:25], v[26:27], off offset:-4096
	s_nop 0
	global_load_dwordx4 v[26:29], v[26:27], off
	s_nop 0
	global_load_dwordx4 v[48:51], v[36:37], off offset:-4096
	s_nop 0
	global_load_dwordx4 v[36:39], v[36:37], off
	s_nop 0
	global_load_dwordx4 v[52:55], v[56:57], off offset:-4096
	s_nop 0
	global_load_dwordx4 v[56:59], v[56:57], off
	s_load_dwordx2 s[6:7], s[30:31], 0x140
	global_load_dwordx4 v[64:67], v[64:65], off
	v_readlane_b32 s1, v249, 2
	s_andn2_b32 s1, s1, 63
	v_and_b32_e32 v132, 0x70, v34
	v_or_b32_e32 v70, s1, v160
	v_add_u32_e32 v34, 0x200, v70
	s_add_i32 s8, s2, 0
	v_ashrrev_i32_e32 v135, 3, v34
	v_add_u32_e32 v34, 0x400, v70
	s_waitcnt lgkmcnt(0)
	s_add_u32 s4, s6, 0x4800000
	v_ashrrev_i32_e32 v137, 3, v34
	v_add_u32_e32 v34, 0x600, v70
	s_addc_u32 s5, s7, 0
	v_ashrrev_i32_e32 v1, 3, v70
	v_ashrrev_i32_e32 v139, 3, v34
	v_lshlrev_b32_e32 v68, 2, v160
	v_mul_u32_u24_e32 v69, 0x240, v160
	v_add_u32_e32 v71, 0, v132
	s_add_u32 s1, s6, 0xc800000
	v_mul_lo_u32 v72, v1, s75
	v_mul_lo_u32 v73, v135, s75
	v_mul_lo_u32 v74, v137, s75
	v_mul_lo_u32 v70, v139, s75
	v_mov_b32_e32 v133, v35
	s_addc_u32 s3, s7, 0
	v_and_b32_e32 v134, 0x7f, v1
	v_and_b32_e32 v136, 0x7f, v135
	v_and_b32_e32 v138, 0x7f, v137
	v_and_b32_e32 v140, 0x7f, v139
	v_lshlrev_b32_e32 v34, 2, v68
	v_add_u32_e32 v141, s8, v69
	v_add_u32_e32 v150, v71, v72
	v_add_u32_e32 v151, v71, v73
	v_add_u32_e32 v152, v71, v74
	v_add_u32_e32 v153, v71, v70
	v_readlane_b32 s8, v250, 2
	v_readlane_b32 s9, v252, 27
	v_readlane_b32 s10, v250, 1
	s_branch .LBB0_2665
